# MoE start-up weight images (first 16 gate_up + 16 down groups per queue) pre-converted during in_proj, staggered one item per workgroup; start-up fillers removed; K-loop waits counted per phase (vmcnt
# speedup vs baseline: 1.0311x; 1.0311x over previous
; #define LAS3 __attribute__((address_space(3)))
; #define G_SCHED __builtin_amdgcn_sched_barrier(0)
; __device__ __forceinline__ int lane_id() { int r; asm volatile("v_mbcnt_lo_u32_b32 %0, -1, 0\n\tv_mbcnt_hi_u32_b32 %0, -1, %0" : "=v"(r)); return r; }
; #define CI_LOAD(R, kt) do { _Pragma("unroll") for (int _j = 0; _j < 16; ++_j) R[_j] = __builtin_nontemporal_load((const f32x4*)(src + (size_t)((kt) * 128 + _j) * LDB)); } while (0)
; template <int LDB>
; __device__ __forceinline__ void convert_image(const float* __restrict__ W, int col0, int col1, unsigned char* __restrict__ img, LAS3 char* lds, int wid) {
;     int lane = lane_id(); asm volatile("" : "+v"(lane));
;     const int n4 = lane, half = n4 >> 5, nloc = (n4 & 31) * 4;
;     const float* src = W + (size_t)(wid * 16) * LDB + ((n4 < 32) ? col0 + n4 * 4 : col1 + (n4 - 32) * 4);
;     const unsigned cpo = (unsigned)(wid * 4096 + lane * 16);
;     ...
;     f32x4 ra[16], rb[16];
;     CI_LOAD(ra, 0);
;     for (int kt = 0; kt < 16; kt += 2) {
;         CI_LOAD(rb, kt + 1); G_SCHED;
; __global__ void __launch_bounds__(512, 2) k_mega(Params p) {
;     ...
;     { GemmArgs g{}; g.A = p.xn; g.C = p.proj; g.R = (const float*)p.proj2;
;       for (int u = vb; u < 32 * 16 + 256; u += nb) {
;           int pm, pn, kh = -1;
;           if (nb == 256) { const int r = u >> 8, x = (u >> 5) & 7, j = u & 31; pm = 8 * (x & 3) + (j & 7);
;               if (u < 32 * 16) pn = 8 * r + 4 * (x >> 2) + (j >> 3); else { pn = 16 + (j >> 3); kh = x >> 2; } }
;           else if (u < 32 * 16) { pm = u & 31; pn = u >> 5; }
;           else { const int v = u - 32 * 16; pn = 16 + (v >> 6); pm = v & 31; kh = (v >> 5) & 1; }
;           gemm_tile_img<0>(g, pm, pn, 0, 0, T, lds, wid, p.img_in + (size_t)pn * 1048576, TileSync{}, kh); } }
.LBB0_75:
	s_cmpk_lg_i32 s80, 0x100
	s_cbranch_scc1 .Lpc_skip
	s_and_b32 s0, s35, 7
	s_cmp_gt_u32 s0, 2
	s_cselect_b32 s1, 1, 0
	s_cmp_gt_u32 s0, 5
	s_cselect_b32 s4, 1, 0
	s_add_i32 s1, s1, s4
	s_lshr_b32 s0, s87, 8
	s_cmp_lg_u32 s0, s1
	s_cbranch_scc1 .Lpc_skip
	v_readlane_b32 s0, v254, 18
	v_readlane_b32 s1, v254, 19
	s_lshr_b32 s100, s35, 5
	s_and_b32 s101, s35, 31
	s_sub_u32 s88, s101, 16
	s_lshr_b32 s4, s88, 3
	s_lshl_b32 s4, s4, 3
	s_add_u32 s4, s4, s100
	s_and_b32 s5, s88, 7
	s_cmp_lt_u32 s101, 16
	s_cselect_b32 vcc_lo, 1, 0
	s_cselect_b32 s4, s100, s4
	s_cselect_b32 s5, s101, s5
	s_sub_u32 s0, s0, 0x140
	s_subb_u32 s1, s1, 0
	s_lshl_b32 s6, vcc_lo, 4
	s_sub_u32 s6, 0x80, s6
	s_lshl_b32 s88, vcc_lo, 3
	s_sub_u32 s88, 0x120, s88
	s_load_dwordx2 s[100:101], s[0:1], s6
	s_load_dwordx2 s[6:7], s[0:1], s88
	s_load_dwordx2 s[0:1], s[0:1], 0x128
	s_waitcnt lgkmcnt(0)
	s_add_u32 s88, vcc_lo, 24
	s_lshl_b32 s88, s4, s88
	s_add_u32 s100, s100, s88
	s_addc_u32 s101, s101, 0
	s_sub_u32 s88, 10, vcc_lo
	s_lshl_b32 s88, s5, s88
	s_add_u32 s100, s100, s88
	s_addc_u32 s101, s101, 0
	s_lshr_b32 vcc_hi, s75, 6
	s_add_u32 s88, vcc_lo, 17
	s_lshl_b32 s88, vcc_hi, s88
	s_add_u32 s100, s100, s88
	s_addc_u32 s101, s101, 0
	s_add_u32 s88, vcc_lo, 3
	s_lshl_b32 s88, s4, s88
	s_add_u32 s88, s88, s5
	s_lshl_b32 s4, s88, 19
	s_add_u32 s6, s6, s4
	s_addc_u32 s7, s7, 0
	s_xor_b32 s4, vcc_lo, 1
	s_lshl_b32 s4, s4, 9
	s_add_u32 s4, s4, s88
	s_lshl_b32 s4, s4, 2
	s_add_u32 s0, s0, s4
	s_addc_u32 s1, s1, 0
	v_mbcnt_lo_u32_b32 v131, -1, 0
	v_mbcnt_hi_u32_b32 v131, -1, v131
	s_add_u32 s4, vcc_lo, 13
	s_lshl_b32 s5, 1, s4
	s_lshl_b32 s88, vcc_lo, 2
	s_add_u32 s88, s88, 9
	s_lshl_b32 s88, 1, s88
	v_and_b32_e32 v132, 31, v131
	v_lshrrev_b32_e32 v150, 5, v131
	v_lshlrev_b32_e32 v132, 4, v132
	v_mad_u32_u24 v132, v150, s88, v132
	v_add_u32_e32 v133, s5, v132
	v_add_u32_e32 v134, s5, v133
	v_add_u32_e32 v135, s5, v134
	v_add_u32_e32 v136, s5, v135
	v_add_u32_e32 v137, s5, v136
	v_add_u32_e32 v138, s5, v137
	v_add_u32_e32 v139, s5, v138
	v_add_u32_e32 v140, s5, v139
	v_add_u32_e32 v141, s5, v140
	v_add_u32_e32 v142, s5, v141
	v_add_u32_e32 v143, s5, v142
	v_add_u32_e32 v144, s5, v143
	v_add_u32_e32 v145, s5, v144
	v_add_u32_e32 v146, s5, v145
	v_add_u32_e32 v147, s5, v146
	v_and_b32_e32 v151, 3, v131
	v_lshlrev_b32_e32 v151, 1, v151
	v_xor_b32_e32 v148, vcc_hi, v151
	v_or_b32_e32 v151, 1, v151
	v_xor_b32_e32 v149, vcc_hi, v151
	v_lshlrev_b32_e32 v148, 4, v148
	v_lshlrev_b32_e32 v149, 4, v149
	v_and_b32_e32 v151, 31, v131
	v_lshlrev_b32_e32 v151, 9, v151
	v_lshl_add_u32 v151, v150, 14, v151
	v_add_u32_e32 v148, v148, v151
	v_add_u32_e32 v149, v149, v151
	v_add_u32_e32 v149, 0x100, v149
	v_lshlrev_b32_e32 v150, 4, v131
	s_lshl_b32 s4, vcc_hi, 12
	v_add_u32_e32 v150, s4, v150
	s_lshl_b32 s88, s5, 7
	s_mov_b32 s5, 0x3b800000
	global_load_dwordx4 v[0:3], v132, s[100:101] nt
	global_load_dwordx4 v[4:7], v133, s[100:101] nt
	global_load_dwordx4 v[8:11], v134, s[100:101] nt
	global_load_dwordx4 v[12:15], v135, s[100:101] nt
	global_load_dwordx4 v[16:19], v136, s[100:101] nt
	global_load_dwordx4 v[20:23], v137, s[100:101] nt
	global_load_dwordx4 v[24:27], v138, s[100:101] nt
	global_load_dwordx4 v[28:31], v139, s[100:101] nt
	global_load_dwordx4 v[32:35], v140, s[100:101] nt
	global_load_dwordx4 v[36:39], v141, s[100:101] nt
	global_load_dwordx4 v[40:43], v142, s[100:101] nt
	global_load_dwordx4 v[44:47], v143, s[100:101] nt
	global_load_dwordx4 v[48:51], v144, s[100:101] nt
	global_load_dwordx4 v[52:55], v145, s[100:101] nt
	global_load_dwordx4 v[56:59], v146, s[100:101] nt
	global_load_dwordx4 v[60:63], v147, s[100:101] nt
	s_add_u32 s100, s100, s88
	s_addc_u32 s101, s101, 0
	global_load_dwordx4 v[64:67], v132, s[100:101] nt
	global_load_dwordx4 v[68:71], v133, s[100:101] nt
	global_load_dwordx4 v[72:75], v134, s[100:101] nt
	global_load_dwordx4 v[76:79], v135, s[100:101] nt
	global_load_dwordx4 v[80:83], v136, s[100:101] nt
	global_load_dwordx4 v[84:87], v137, s[100:101] nt
	global_load_dwordx4 v[88:91], v138, s[100:101] nt
	global_load_dwordx4 v[92:95], v139, s[100:101] nt
	global_load_dwordx4 v[96:99], v140, s[100:101] nt
	global_load_dwordx4 v[100:103], v141, s[100:101] nt
	global_load_dwordx4 v[104:107], v142, s[100:101] nt
	global_load_dwordx4 v[108:111], v143, s[100:101] nt
	global_load_dwordx4 v[112:115], v144, s[100:101] nt
	global_load_dwordx4 v[116:119], v145, s[100:101] nt
	global_load_dwordx4 v[120:123], v146, s[100:101] nt
	global_load_dwordx4 v[124:127], v147, s[100:101] nt
	s_waitcnt vmcnt(16)
	v_cvt_scalef32_pk_fp8_f32 v152, v0, v4, s5
	v_cvt_scalef32_pk_fp8_f32 v156, v1, v5, s5
	v_cvt_scalef32_pk_fp8_f32 v160, v2, v6, s5
	v_cvt_scalef32_pk_fp8_f32 v164, v3, v7, s5
	v_cvt_scalef32_pk_fp8_f32 v153, v16, v20, s5
	v_cvt_scalef32_pk_fp8_f32 v157, v17, v21, s5
	v_cvt_scalef32_pk_fp8_f32 v161, v18, v22, s5
	v_cvt_scalef32_pk_fp8_f32 v165, v19, v23, s5
	v_cvt_scalef32_pk_fp8_f32 v154, v32, v36, s5
	v_cvt_scalef32_pk_fp8_f32 v158, v33, v37, s5
	v_cvt_scalef32_pk_fp8_f32 v162, v34, v38, s5
	v_cvt_scalef32_pk_fp8_f32 v166, v35, v39, s5
	v_cvt_scalef32_pk_fp8_f32 v155, v48, v52, s5
	v_cvt_scalef32_pk_fp8_f32 v159, v49, v53, s5
	v_cvt_scalef32_pk_fp8_f32 v163, v50, v54, s5
	v_cvt_scalef32_pk_fp8_f32 v167, v51, v55, s5
	v_cvt_scalef32_pk_fp8_f32 v152, v8, v12, s5 op_sel:[0,0,0,1]
	v_cvt_scalef32_pk_fp8_f32 v156, v9, v13, s5 op_sel:[0,0,0,1]
	v_cvt_scalef32_pk_fp8_f32 v160, v10, v14, s5 op_sel:[0,0,0,1]
	v_cvt_scalef32_pk_fp8_f32 v164, v11, v15, s5 op_sel:[0,0,0,1]
	v_cvt_scalef32_pk_fp8_f32 v153, v24, v28, s5 op_sel:[0,0,0,1]
	v_cvt_scalef32_pk_fp8_f32 v157, v25, v29, s5 op_sel:[0,0,0,1]
	v_cvt_scalef32_pk_fp8_f32 v161, v26, v30, s5 op_sel:[0,0,0,1]
	v_cvt_scalef32_pk_fp8_f32 v165, v27, v31, s5 op_sel:[0,0,0,1]
	v_cvt_scalef32_pk_fp8_f32 v154, v40, v44, s5 op_sel:[0,0,0,1]
	v_cvt_scalef32_pk_fp8_f32 v158, v41, v45, s5 op_sel:[0,0,0,1]
	v_cvt_scalef32_pk_fp8_f32 v162, v42, v46, s5 op_sel:[0,0,0,1]
	v_cvt_scalef32_pk_fp8_f32 v166, v43, v47, s5 op_sel:[0,0,0,1]
	v_cvt_scalef32_pk_fp8_f32 v155, v56, v60, s5 op_sel:[0,0,0,1]
	v_cvt_scalef32_pk_fp8_f32 v159, v57, v61, s5 op_sel:[0,0,0,1]
	v_cvt_scalef32_pk_fp8_f32 v163, v58, v62, s5 op_sel:[0,0,0,1]
	v_cvt_scalef32_pk_fp8_f32 v167, v59, v63, s5 op_sel:[0,0,0,1]
	s_nop 0
	ds_write_b128 v148, v[152:155] offset:0
	ds_write_b128 v148, v[156:159] offset:128
	ds_write_b128 v149, v[160:163] offset:0
	ds_write_b128 v149, v[164:167] offset:128
	s_waitcnt lgkmcnt(0)
	s_barrier
; #define G_SCHED __builtin_amdgcn_sched_barrier(0)
; #define CI_LOAD(R, kt) do { _Pragma("unroll") for (int _j = 0; _j < 16; ++_j) R[_j] = __builtin_nontemporal_load((const f32x4*)(src + (size_t)((kt) * 128 + _j) * LDB)); } while (0)
; template <int LDB>
; __device__ __forceinline__ void convert_image(const float* __restrict__ W, int col0, int col1, unsigned char* __restrict__ img, LAS3 char* lds, int wid) {
;     ...
;     f32x4 ra[16], rb[16];
;     CI_LOAD(ra, 0);
;     for (int kt = 0; kt < 16; kt += 2) {
;         CI_LOAD(rb, kt + 1); G_SCHED;
;         CI_CONV(ra, kt); G_SCHED;
;         CI_LOAD(ra, (kt + 2 < 16) ? kt + 2 : 15); G_SCHED;
;         CI_CONV(rb, kt + 1); G_SCHED;
;     }
	ds_read_b128 v[168:171], v150 offset:0
	ds_read_b128 v[172:175], v150 offset:1024
	ds_read_b128 v[176:179], v150 offset:2048
	ds_read_b128 v[180:183], v150 offset:3072
	s_waitcnt lgkmcnt(3)
	global_store_dwordx4 v150, v[168:171], s[6:7] sc1
	s_waitcnt lgkmcnt(2)
	global_store_dwordx4 v150, v[172:175], s[6:7] offset:1024 sc1
	s_waitcnt lgkmcnt(1)
	global_store_dwordx4 v150, v[176:179], s[6:7] offset:2048 sc1
	s_waitcnt lgkmcnt(0)
	global_store_dwordx4 v150, v[180:183], s[6:7] offset:3072 sc1
	s_add_u32 s6, s6, 0x8000
	s_addc_u32 s7, s7, 0
	s_add_u32 s100, s100, s88
	s_addc_u32 s101, s101, 0
	global_load_dwordx4 v[0:3], v132, s[100:101] nt
	global_load_dwordx4 v[4:7], v133, s[100:101] nt
	global_load_dwordx4 v[8:11], v134, s[100:101] nt
	global_load_dwordx4 v[12:15], v135, s[100:101] nt
	global_load_dwordx4 v[16:19], v136, s[100:101] nt
	global_load_dwordx4 v[20:23], v137, s[100:101] nt
	global_load_dwordx4 v[24:27], v138, s[100:101] nt
	global_load_dwordx4 v[28:31], v139, s[100:101] nt
	global_load_dwordx4 v[32:35], v140, s[100:101] nt
	global_load_dwordx4 v[36:39], v141, s[100:101] nt
	global_load_dwordx4 v[40:43], v142, s[100:101] nt
	global_load_dwordx4 v[44:47], v143, s[100:101] nt
	global_load_dwordx4 v[48:51], v144, s[100:101] nt
	global_load_dwordx4 v[52:55], v145, s[100:101] nt
	global_load_dwordx4 v[56:59], v146, s[100:101] nt
	global_load_dwordx4 v[60:63], v147, s[100:101] nt
	s_waitcnt vmcnt(20)
	v_cvt_scalef32_pk_fp8_f32 v152, v64, v68, s5
	v_cvt_scalef32_pk_fp8_f32 v156, v65, v69, s5
	v_cvt_scalef32_pk_fp8_f32 v160, v66, v70, s5
	v_cvt_scalef32_pk_fp8_f32 v164, v67, v71, s5
	v_cvt_scalef32_pk_fp8_f32 v153, v80, v84, s5
	v_cvt_scalef32_pk_fp8_f32 v157, v81, v85, s5
	v_cvt_scalef32_pk_fp8_f32 v161, v82, v86, s5
	v_cvt_scalef32_pk_fp8_f32 v165, v83, v87, s5
	v_cvt_scalef32_pk_fp8_f32 v154, v96, v100, s5
	v_cvt_scalef32_pk_fp8_f32 v158, v97, v101, s5
	v_cvt_scalef32_pk_fp8_f32 v162, v98, v102, s5
	v_cvt_scalef32_pk_fp8_f32 v166, v99, v103, s5
	v_cvt_scalef32_pk_fp8_f32 v155, v112, v116, s5
	v_cvt_scalef32_pk_fp8_f32 v159, v113, v117, s5
	v_cvt_scalef32_pk_fp8_f32 v163, v114, v118, s5
	v_cvt_scalef32_pk_fp8_f32 v167, v115, v119, s5
	v_cvt_scalef32_pk_fp8_f32 v152, v72, v76, s5 op_sel:[0,0,0,1]
	v_cvt_scalef32_pk_fp8_f32 v156, v73, v77, s5 op_sel:[0,0,0,1]
	v_cvt_scalef32_pk_fp8_f32 v160, v74, v78, s5 op_sel:[0,0,0,1]
	v_cvt_scalef32_pk_fp8_f32 v164, v75, v79, s5 op_sel:[0,0,0,1]
	v_cvt_scalef32_pk_fp8_f32 v153, v88, v92, s5 op_sel:[0,0,0,1]
	v_cvt_scalef32_pk_fp8_f32 v157, v89, v93, s5 op_sel:[0,0,0,1]
	v_cvt_scalef32_pk_fp8_f32 v161, v90, v94, s5 op_sel:[0,0,0,1]
	v_cvt_scalef32_pk_fp8_f32 v165, v91, v95, s5 op_sel:[0,0,0,1]
	v_cvt_scalef32_pk_fp8_f32 v154, v104, v108, s5 op_sel:[0,0,0,1]
	v_cvt_scalef32_pk_fp8_f32 v158, v105, v109, s5 op_sel:[0,0,0,1]
	v_cvt_scalef32_pk_fp8_f32 v162, v106, v110, s5 op_sel:[0,0,0,1]
	v_cvt_scalef32_pk_fp8_f32 v166, v107, v111, s5 op_sel:[0,0,0,1]
	v_cvt_scalef32_pk_fp8_f32 v155, v120, v124, s5 op_sel:[0,0,0,1]
	v_cvt_scalef32_pk_fp8_f32 v159, v121, v125, s5 op_sel:[0,0,0,1]
	v_cvt_scalef32_pk_fp8_f32 v163, v122, v126, s5 op_sel:[0,0,0,1]
	v_cvt_scalef32_pk_fp8_f32 v167, v123, v127, s5 op_sel:[0,0,0,1]
	s_nop 0
	ds_write_b128 v148, v[152:155] offset:32768
	ds_write_b128 v148, v[156:159] offset:32896
	ds_write_b128 v149, v[160:163] offset:32768
	ds_write_b128 v149, v[164:167] offset:32896
	s_waitcnt lgkmcnt(0)
	s_barrier
	ds_read_b128 v[168:171], v150 offset:32768
	ds_read_b128 v[172:175], v150 offset:33792
	ds_read_b128 v[176:179], v150 offset:34816
	ds_read_b128 v[180:183], v150 offset:35840
	s_waitcnt lgkmcnt(3)
	global_store_dwordx4 v150, v[168:171], s[6:7] sc1
	s_waitcnt lgkmcnt(2)
	global_store_dwordx4 v150, v[172:175], s[6:7] offset:1024 sc1
	s_waitcnt lgkmcnt(1)
	global_store_dwordx4 v150, v[176:179], s[6:7] offset:2048 sc1
	s_waitcnt lgkmcnt(0)
	global_store_dwordx4 v150, v[180:183], s[6:7] offset:3072 sc1
	s_add_u32 s6, s6, 0x8000
	s_addc_u32 s7, s7, 0
	s_mov_b32 s4, 6
.Lpc_loop:
	s_add_u32 s100, s100, s88
	s_addc_u32 s101, s101, 0
	global_load_dwordx4 v[64:67], v132, s[100:101] nt
	global_load_dwordx4 v[68:71], v133, s[100:101] nt
	global_load_dwordx4 v[72:75], v134, s[100:101] nt
	global_load_dwordx4 v[76:79], v135, s[100:101] nt
	global_load_dwordx4 v[80:83], v136, s[100:101] nt
	global_load_dwordx4 v[84:87], v137, s[100:101] nt
	global_load_dwordx4 v[88:91], v138, s[100:101] nt
	global_load_dwordx4 v[92:95], v139, s[100:101] nt
	global_load_dwordx4 v[96:99], v140, s[100:101] nt
	global_load_dwordx4 v[100:103], v141, s[100:101] nt
	global_load_dwordx4 v[104:107], v142, s[100:101] nt
	global_load_dwordx4 v[108:111], v143, s[100:101] nt
	global_load_dwordx4 v[112:115], v144, s[100:101] nt
	global_load_dwordx4 v[116:119], v145, s[100:101] nt
	global_load_dwordx4 v[120:123], v146, s[100:101] nt
	global_load_dwordx4 v[124:127], v147, s[100:101] nt
	s_waitcnt vmcnt(20)
	v_cvt_scalef32_pk_fp8_f32 v152, v0, v4, s5
	v_cvt_scalef32_pk_fp8_f32 v156, v1, v5, s5
	v_cvt_scalef32_pk_fp8_f32 v160, v2, v6, s5
	v_cvt_scalef32_pk_fp8_f32 v164, v3, v7, s5
	v_cvt_scalef32_pk_fp8_f32 v153, v16, v20, s5
	v_cvt_scalef32_pk_fp8_f32 v157, v17, v21, s5
	v_cvt_scalef32_pk_fp8_f32 v161, v18, v22, s5
	v_cvt_scalef32_pk_fp8_f32 v165, v19, v23, s5
	v_cvt_scalef32_pk_fp8_f32 v154, v32, v36, s5
	v_cvt_scalef32_pk_fp8_f32 v158, v33, v37, s5
	v_cvt_scalef32_pk_fp8_f32 v162, v34, v38, s5
	v_cvt_scalef32_pk_fp8_f32 v166, v35, v39, s5
	v_cvt_scalef32_pk_fp8_f32 v155, v48, v52, s5
	v_cvt_scalef32_pk_fp8_f32 v159, v49, v53, s5
	v_cvt_scalef32_pk_fp8_f32 v163, v50, v54, s5
	v_cvt_scalef32_pk_fp8_f32 v167, v51, v55, s5
	v_cvt_scalef32_pk_fp8_f32 v152, v8, v12, s5 op_sel:[0,0,0,1]
	v_cvt_scalef32_pk_fp8_f32 v156, v9, v13, s5 op_sel:[0,0,0,1]
	v_cvt_scalef32_pk_fp8_f32 v160, v10, v14, s5 op_sel:[0,0,0,1]
	v_cvt_scalef32_pk_fp8_f32 v164, v11, v15, s5 op_sel:[0,0,0,1]
	v_cvt_scalef32_pk_fp8_f32 v153, v24, v28, s5 op_sel:[0,0,0,1]
	v_cvt_scalef32_pk_fp8_f32 v157, v25, v29, s5 op_sel:[0,0,0,1]
	v_cvt_scalef32_pk_fp8_f32 v161, v26, v30, s5 op_sel:[0,0,0,1]
	v_cvt_scalef32_pk_fp8_f32 v165, v27, v31, s5 op_sel:[0,0,0,1]
	v_cvt_scalef32_pk_fp8_f32 v154, v40, v44, s5 op_sel:[0,0,0,1]
	v_cvt_scalef32_pk_fp8_f32 v158, v41, v45, s5 op_sel:[0,0,0,1]
	v_cvt_scalef32_pk_fp8_f32 v162, v42, v46, s5 op_sel:[0,0,0,1]
	v_cvt_scalef32_pk_fp8_f32 v166, v43, v47, s5 op_sel:[0,0,0,1]
	v_cvt_scalef32_pk_fp8_f32 v155, v56, v60, s5 op_sel:[0,0,0,1]
	v_cvt_scalef32_pk_fp8_f32 v159, v57, v61, s5 op_sel:[0,0,0,1]
	v_cvt_scalef32_pk_fp8_f32 v163, v58, v62, s5 op_sel:[0,0,0,1]
	v_cvt_scalef32_pk_fp8_f32 v167, v59, v63, s5 op_sel:[0,0,0,1]
	s_nop 0
	ds_write_b128 v148, v[152:155] offset:0
	ds_write_b128 v148, v[156:159] offset:128
	ds_write_b128 v149, v[160:163] offset:0
	ds_write_b128 v149, v[164:167] offset:128
	s_waitcnt lgkmcnt(0)
	s_barrier
; #define G_SCHED __builtin_amdgcn_sched_barrier(0)
; #define CI_LOAD(R, kt) do { _Pragma("unroll") for (int _j = 0; _j < 16; ++_j) R[_j] = __builtin_nontemporal_load((const f32x4*)(src + (size_t)((kt) * 128 + _j) * LDB)); } while (0)
; template <int LDB>
; __device__ __forceinline__ void convert_image(const float* __restrict__ W, int col0, int col1, unsigned char* __restrict__ img, LAS3 char* lds, int wid) {
;     ...
;     f32x4 ra[16], rb[16];
;     CI_LOAD(ra, 0);
;     for (int kt = 0; kt < 16; kt += 2) {
;         CI_LOAD(rb, kt + 1); G_SCHED;
;         CI_CONV(ra, kt); G_SCHED;
;         CI_LOAD(ra, (kt + 2 < 16) ? kt + 2 : 15); G_SCHED;
;         CI_CONV(rb, kt + 1); G_SCHED;
;     }
	ds_read_b128 v[168:171], v150 offset:0
	ds_read_b128 v[172:175], v150 offset:1024
	ds_read_b128 v[176:179], v150 offset:2048
	ds_read_b128 v[180:183], v150 offset:3072
	s_waitcnt lgkmcnt(3)
	global_store_dwordx4 v150, v[168:171], s[6:7] sc1
	s_waitcnt lgkmcnt(2)
	global_store_dwordx4 v150, v[172:175], s[6:7] offset:1024 sc1
	s_waitcnt lgkmcnt(1)
	global_store_dwordx4 v150, v[176:179], s[6:7] offset:2048 sc1
	s_waitcnt lgkmcnt(0)
	global_store_dwordx4 v150, v[180:183], s[6:7] offset:3072 sc1
	s_add_u32 s6, s6, 0x8000
	s_addc_u32 s7, s7, 0
	s_add_u32 s100, s100, s88
	s_addc_u32 s101, s101, 0
	global_load_dwordx4 v[0:3], v132, s[100:101] nt
	global_load_dwordx4 v[4:7], v133, s[100:101] nt
	global_load_dwordx4 v[8:11], v134, s[100:101] nt
	global_load_dwordx4 v[12:15], v135, s[100:101] nt
	global_load_dwordx4 v[16:19], v136, s[100:101] nt
	global_load_dwordx4 v[20:23], v137, s[100:101] nt
	global_load_dwordx4 v[24:27], v138, s[100:101] nt
	global_load_dwordx4 v[28:31], v139, s[100:101] nt
	global_load_dwordx4 v[32:35], v140, s[100:101] nt
	global_load_dwordx4 v[36:39], v141, s[100:101] nt
	global_load_dwordx4 v[40:43], v142, s[100:101] nt
	global_load_dwordx4 v[44:47], v143, s[100:101] nt
	global_load_dwordx4 v[48:51], v144, s[100:101] nt
	global_load_dwordx4 v[52:55], v145, s[100:101] nt
	global_load_dwordx4 v[56:59], v146, s[100:101] nt
	global_load_dwordx4 v[60:63], v147, s[100:101] nt
	s_waitcnt vmcnt(20)
	v_cvt_scalef32_pk_fp8_f32 v152, v64, v68, s5
	v_cvt_scalef32_pk_fp8_f32 v156, v65, v69, s5
	v_cvt_scalef32_pk_fp8_f32 v160, v66, v70, s5
	v_cvt_scalef32_pk_fp8_f32 v164, v67, v71, s5
	v_cvt_scalef32_pk_fp8_f32 v153, v80, v84, s5
	v_cvt_scalef32_pk_fp8_f32 v157, v81, v85, s5
	v_cvt_scalef32_pk_fp8_f32 v161, v82, v86, s5
	v_cvt_scalef32_pk_fp8_f32 v165, v83, v87, s5
	v_cvt_scalef32_pk_fp8_f32 v154, v96, v100, s5
	v_cvt_scalef32_pk_fp8_f32 v158, v97, v101, s5
	v_cvt_scalef32_pk_fp8_f32 v162, v98, v102, s5
	v_cvt_scalef32_pk_fp8_f32 v166, v99, v103, s5
	v_cvt_scalef32_pk_fp8_f32 v155, v112, v116, s5
	v_cvt_scalef32_pk_fp8_f32 v159, v113, v117, s5
	v_cvt_scalef32_pk_fp8_f32 v163, v114, v118, s5
	v_cvt_scalef32_pk_fp8_f32 v167, v115, v119, s5
	v_cvt_scalef32_pk_fp8_f32 v152, v72, v76, s5 op_sel:[0,0,0,1]
	v_cvt_scalef32_pk_fp8_f32 v156, v73, v77, s5 op_sel:[0,0,0,1]
	v_cvt_scalef32_pk_fp8_f32 v160, v74, v78, s5 op_sel:[0,0,0,1]
	v_cvt_scalef32_pk_fp8_f32 v164, v75, v79, s5 op_sel:[0,0,0,1]
	v_cvt_scalef32_pk_fp8_f32 v153, v88, v92, s5 op_sel:[0,0,0,1]
	v_cvt_scalef32_pk_fp8_f32 v157, v89, v93, s5 op_sel:[0,0,0,1]
	v_cvt_scalef32_pk_fp8_f32 v161, v90, v94, s5 op_sel:[0,0,0,1]
	v_cvt_scalef32_pk_fp8_f32 v165, v91, v95, s5 op_sel:[0,0,0,1]
	v_cvt_scalef32_pk_fp8_f32 v154, v104, v108, s5 op_sel:[0,0,0,1]
	v_cvt_scalef32_pk_fp8_f32 v158, v105, v109, s5 op_sel:[0,0,0,1]
	v_cvt_scalef32_pk_fp8_f32 v162, v106, v110, s5 op_sel:[0,0,0,1]
	v_cvt_scalef32_pk_fp8_f32 v166, v107, v111, s5 op_sel:[0,0,0,1]
	v_cvt_scalef32_pk_fp8_f32 v155, v120, v124, s5 op_sel:[0,0,0,1]
	v_cvt_scalef32_pk_fp8_f32 v159, v121, v125, s5 op_sel:[0,0,0,1]
	v_cvt_scalef32_pk_fp8_f32 v163, v122, v126, s5 op_sel:[0,0,0,1]
	v_cvt_scalef32_pk_fp8_f32 v167, v123, v127, s5 op_sel:[0,0,0,1]
	s_nop 0
	ds_write_b128 v148, v[152:155] offset:32768
	ds_write_b128 v148, v[156:159] offset:32896
	ds_write_b128 v149, v[160:163] offset:32768
	ds_write_b128 v149, v[164:167] offset:32896
	s_waitcnt lgkmcnt(0)
	s_barrier
	ds_read_b128 v[168:171], v150 offset:32768
	ds_read_b128 v[172:175], v150 offset:33792
	ds_read_b128 v[176:179], v150 offset:34816
	ds_read_b128 v[180:183], v150 offset:35840
	s_waitcnt lgkmcnt(3)
	global_store_dwordx4 v150, v[168:171], s[6:7] sc1
	s_waitcnt lgkmcnt(2)
	global_store_dwordx4 v150, v[172:175], s[6:7] offset:1024 sc1
	s_waitcnt lgkmcnt(1)
	global_store_dwordx4 v150, v[176:179], s[6:7] offset:2048 sc1
	s_waitcnt lgkmcnt(0)
	global_store_dwordx4 v150, v[180:183], s[6:7] offset:3072 sc1
	s_add_u32 s6, s6, 0x8000
	s_addc_u32 s7, s7, 0
	s_sub_u32 s4, s4, 1
	s_cmp_lg_u32 s4, 0
	s_cbranch_scc1 .Lpc_loop
; #define G_SCHED __builtin_amdgcn_sched_barrier(0)
; #define CI_LOAD(R, kt) do { _Pragma("unroll") for (int _j = 0; _j < 16; ++_j) R[_j] = __builtin_nontemporal_load((const f32x4*)(src + (size_t)((kt) * 128 + _j) * LDB)); } while (0)
; #define LD_WAIT(r) asm volatile("s_waitcnt vmcnt(0)" : "+v"(r) :: "memory")
; template <int LDB>
; __device__ __forceinline__ void convert_image(const float* __restrict__ W, int col0, int col1, unsigned char* __restrict__ img, LAS3 char* lds, int wid) {
;     ...
;     f32x4 ra[16], rb[16];
;     CI_LOAD(ra, 0);
;     for (int kt = 0; kt < 16; kt += 2) {
;         CI_LOAD(rb, kt + 1); G_SCHED;
;         CI_CONV(ra, kt); G_SCHED;
;         CI_LOAD(ra, (kt + 2 < 16) ? kt + 2 : 15); G_SCHED;
;         CI_CONV(rb, kt + 1); G_SCHED;
;     }
;     asm volatile("s_waitcnt vmcnt(0)" ::: "memory");
;     __syncthreads();
; template <int EPI>
; __device__ __forceinline__ int* moe_phase(const Params& p, LAS3 char* lds, int wid, int* pend_in) {
;     ...
;                 if (t0 == 0) { __hip_atomic_store(p.flag + NE * 16 + e * 8 + pn, 1, __ATOMIC_RELAXED, __HIP_MEMORY_SCOPE_AGENT); unsigned c0 = inc_early(&qctr[qq]); LD_WAIT(c0); slot[par ^ 1] = ((unsigned)qq << 20) | c0; }
	s_add_u32 s100, s100, s88
	s_addc_u32 s101, s101, 0
	global_load_dwordx4 v[64:67], v132, s[100:101] nt
	global_load_dwordx4 v[68:71], v133, s[100:101] nt
	global_load_dwordx4 v[72:75], v134, s[100:101] nt
	global_load_dwordx4 v[76:79], v135, s[100:101] nt
	global_load_dwordx4 v[80:83], v136, s[100:101] nt
	global_load_dwordx4 v[84:87], v137, s[100:101] nt
	global_load_dwordx4 v[88:91], v138, s[100:101] nt
	global_load_dwordx4 v[92:95], v139, s[100:101] nt
	global_load_dwordx4 v[96:99], v140, s[100:101] nt
	global_load_dwordx4 v[100:103], v141, s[100:101] nt
	global_load_dwordx4 v[104:107], v142, s[100:101] nt
	global_load_dwordx4 v[108:111], v143, s[100:101] nt
	global_load_dwordx4 v[112:115], v144, s[100:101] nt
	global_load_dwordx4 v[116:119], v145, s[100:101] nt
	global_load_dwordx4 v[120:123], v146, s[100:101] nt
	global_load_dwordx4 v[124:127], v147, s[100:101] nt
	s_waitcnt vmcnt(20)
	v_cvt_scalef32_pk_fp8_f32 v152, v0, v4, s5
	v_cvt_scalef32_pk_fp8_f32 v156, v1, v5, s5
	v_cvt_scalef32_pk_fp8_f32 v160, v2, v6, s5
	v_cvt_scalef32_pk_fp8_f32 v164, v3, v7, s5
	v_cvt_scalef32_pk_fp8_f32 v153, v16, v20, s5
	v_cvt_scalef32_pk_fp8_f32 v157, v17, v21, s5
	v_cvt_scalef32_pk_fp8_f32 v161, v18, v22, s5
	v_cvt_scalef32_pk_fp8_f32 v165, v19, v23, s5
	v_cvt_scalef32_pk_fp8_f32 v154, v32, v36, s5
	v_cvt_scalef32_pk_fp8_f32 v158, v33, v37, s5
	v_cvt_scalef32_pk_fp8_f32 v162, v34, v38, s5
	v_cvt_scalef32_pk_fp8_f32 v166, v35, v39, s5
	v_cvt_scalef32_pk_fp8_f32 v155, v48, v52, s5
	v_cvt_scalef32_pk_fp8_f32 v159, v49, v53, s5
	v_cvt_scalef32_pk_fp8_f32 v163, v50, v54, s5
	v_cvt_scalef32_pk_fp8_f32 v167, v51, v55, s5
	v_cvt_scalef32_pk_fp8_f32 v152, v8, v12, s5 op_sel:[0,0,0,1]
	v_cvt_scalef32_pk_fp8_f32 v156, v9, v13, s5 op_sel:[0,0,0,1]
	v_cvt_scalef32_pk_fp8_f32 v160, v10, v14, s5 op_sel:[0,0,0,1]
	v_cvt_scalef32_pk_fp8_f32 v164, v11, v15, s5 op_sel:[0,0,0,1]
	v_cvt_scalef32_pk_fp8_f32 v153, v24, v28, s5 op_sel:[0,0,0,1]
	v_cvt_scalef32_pk_fp8_f32 v157, v25, v29, s5 op_sel:[0,0,0,1]
	v_cvt_scalef32_pk_fp8_f32 v161, v26, v30, s5 op_sel:[0,0,0,1]
	v_cvt_scalef32_pk_fp8_f32 v165, v27, v31, s5 op_sel:[0,0,0,1]
	v_cvt_scalef32_pk_fp8_f32 v154, v40, v44, s5 op_sel:[0,0,0,1]
	v_cvt_scalef32_pk_fp8_f32 v158, v41, v45, s5 op_sel:[0,0,0,1]
	v_cvt_scalef32_pk_fp8_f32 v162, v42, v46, s5 op_sel:[0,0,0,1]
	v_cvt_scalef32_pk_fp8_f32 v166, v43, v47, s5 op_sel:[0,0,0,1]
	v_cvt_scalef32_pk_fp8_f32 v155, v56, v60, s5 op_sel:[0,0,0,1]
	v_cvt_scalef32_pk_fp8_f32 v159, v57, v61, s5 op_sel:[0,0,0,1]
	v_cvt_scalef32_pk_fp8_f32 v163, v58, v62, s5 op_sel:[0,0,0,1]
	v_cvt_scalef32_pk_fp8_f32 v167, v59, v63, s5 op_sel:[0,0,0,1]
	s_nop 0
	ds_write_b128 v148, v[152:155] offset:0
	ds_write_b128 v148, v[156:159] offset:128
	ds_write_b128 v149, v[160:163] offset:0
	ds_write_b128 v149, v[164:167] offset:128
	s_waitcnt lgkmcnt(0)
	s_barrier
	ds_read_b128 v[168:171], v150 offset:0
	ds_read_b128 v[172:175], v150 offset:1024
	ds_read_b128 v[176:179], v150 offset:2048
	ds_read_b128 v[180:183], v150 offset:3072
	s_waitcnt lgkmcnt(3)
	global_store_dwordx4 v150, v[168:171], s[6:7] sc1
	s_waitcnt lgkmcnt(2)
	global_store_dwordx4 v150, v[172:175], s[6:7] offset:1024 sc1
	s_waitcnt lgkmcnt(1)
	global_store_dwordx4 v150, v[176:179], s[6:7] offset:2048 sc1
	s_waitcnt lgkmcnt(0)
	global_store_dwordx4 v150, v[180:183], s[6:7] offset:3072 sc1
	s_add_u32 s6, s6, 0x8000
	s_addc_u32 s7, s7, 0
	s_waitcnt vmcnt(4)
	v_cvt_scalef32_pk_fp8_f32 v152, v64, v68, s5
	v_cvt_scalef32_pk_fp8_f32 v156, v65, v69, s5
	v_cvt_scalef32_pk_fp8_f32 v160, v66, v70, s5
	v_cvt_scalef32_pk_fp8_f32 v164, v67, v71, s5
	v_cvt_scalef32_pk_fp8_f32 v153, v80, v84, s5
	v_cvt_scalef32_pk_fp8_f32 v157, v81, v85, s5
	v_cvt_scalef32_pk_fp8_f32 v161, v82, v86, s5
	v_cvt_scalef32_pk_fp8_f32 v165, v83, v87, s5
	v_cvt_scalef32_pk_fp8_f32 v154, v96, v100, s5
	v_cvt_scalef32_pk_fp8_f32 v158, v97, v101, s5
	v_cvt_scalef32_pk_fp8_f32 v162, v98, v102, s5
	v_cvt_scalef32_pk_fp8_f32 v166, v99, v103, s5
	v_cvt_scalef32_pk_fp8_f32 v155, v112, v116, s5
	v_cvt_scalef32_pk_fp8_f32 v159, v113, v117, s5
	v_cvt_scalef32_pk_fp8_f32 v163, v114, v118, s5
	v_cvt_scalef32_pk_fp8_f32 v167, v115, v119, s5
	v_cvt_scalef32_pk_fp8_f32 v152, v72, v76, s5 op_sel:[0,0,0,1]
	v_cvt_scalef32_pk_fp8_f32 v156, v73, v77, s5 op_sel:[0,0,0,1]
	v_cvt_scalef32_pk_fp8_f32 v160, v74, v78, s5 op_sel:[0,0,0,1]
	v_cvt_scalef32_pk_fp8_f32 v164, v75, v79, s5 op_sel:[0,0,0,1]
	v_cvt_scalef32_pk_fp8_f32 v153, v88, v92, s5 op_sel:[0,0,0,1]
	v_cvt_scalef32_pk_fp8_f32 v157, v89, v93, s5 op_sel:[0,0,0,1]
	v_cvt_scalef32_pk_fp8_f32 v161, v90, v94, s5 op_sel:[0,0,0,1]
	v_cvt_scalef32_pk_fp8_f32 v165, v91, v95, s5 op_sel:[0,0,0,1]
	v_cvt_scalef32_pk_fp8_f32 v154, v104, v108, s5 op_sel:[0,0,0,1]
	v_cvt_scalef32_pk_fp8_f32 v158, v105, v109, s5 op_sel:[0,0,0,1]
	v_cvt_scalef32_pk_fp8_f32 v162, v106, v110, s5 op_sel:[0,0,0,1]
	v_cvt_scalef32_pk_fp8_f32 v166, v107, v111, s5 op_sel:[0,0,0,1]
	v_cvt_scalef32_pk_fp8_f32 v155, v120, v124, s5 op_sel:[0,0,0,1]
	v_cvt_scalef32_pk_fp8_f32 v159, v121, v125, s5 op_sel:[0,0,0,1]
	v_cvt_scalef32_pk_fp8_f32 v163, v122, v126, s5 op_sel:[0,0,0,1]
	v_cvt_scalef32_pk_fp8_f32 v167, v123, v127, s5 op_sel:[0,0,0,1]
	s_nop 0
	ds_write_b128 v148, v[152:155] offset:32768
	ds_write_b128 v148, v[156:159] offset:32896
	ds_write_b128 v149, v[160:163] offset:32768
	ds_write_b128 v149, v[164:167] offset:32896
	s_waitcnt lgkmcnt(0)
	s_barrier
	ds_read_b128 v[168:171], v150 offset:32768
	ds_read_b128 v[172:175], v150 offset:33792
	ds_read_b128 v[176:179], v150 offset:34816
	ds_read_b128 v[180:183], v150 offset:35840
	s_waitcnt lgkmcnt(3)
	global_store_dwordx4 v150, v[168:171], s[6:7] sc1
	s_waitcnt lgkmcnt(2)
	global_store_dwordx4 v150, v[172:175], s[6:7] offset:1024 sc1
	s_waitcnt lgkmcnt(1)
	global_store_dwordx4 v150, v[176:179], s[6:7] offset:2048 sc1
	s_waitcnt lgkmcnt(0)
	global_store_dwordx4 v150, v[180:183], s[6:7] offset:3072 sc1
	s_add_u32 s6, s6, 0x8000
	s_addc_u32 s7, s7, 0
	s_waitcnt vmcnt(0)
	s_barrier
	s_cmp_lg_u32 vcc_hi, 0
	s_cbranch_scc1 .Lpc_skip
	v_mov_b32_e32 v152, 0
	v_mov_b32_e32 v153, 1
	v_cmp_eq_u32_e32 vcc, 0, v131
	s_and_saveexec_b64 s[4:5], vcc
	global_store_dword v152, v153, s[0:1] sc1
	s_mov_b64 exec, s[4:5]

; #define LAS3 __attribute__((address_space(3)))
; template <int EPI>
; __device__ __forceinline__ int* moe_phase(const Params& p, LAS3 char* lds, int wid, int* pend_in) {
;     ...
;       if (t0 < 8) { int a = 0; LAS3 int* pq = pre + t0 * 128;
;           for (int s = 0; s <= NSL; ++s) { pq[s] = a;
;               if (s < NSL) { int nv = (s < NS && mtv[t0 + 8 * (s / NCOL)] > 0) ? 1 : 0; const int sc = s - MOE_LAG;
;                   if (EPI == 2 && s < MOE_LAG3 && mtv[t0 + 8 * (s >> 3)] > 0) nv += 1;
;                   if (sc >= 0 && sc < NS) nv += mtv[t0 + 8 * (sc / NCOL)];
;                   a += nv; } } } }
.LBB0_413:
	v_add_u32_e32 v4, -4, v2
	s_cmp_lt_u32 s6, 64
	ds_write_b32 v4, v3
	s_cselect_b64 s[4:5], -1, 0
	s_cmp_gt_u32 s6, 63
	v_mov_b32_e32 v4, 0
	s_cbranch_scc0 .LBB0_420
	s_cmp_gt_u32 s6, 14
.LBB0_415:
	s_cmp_lt_u32 s6, 15
	s_cbranch_scc0 .LBB0_422

; #define LAS3 __attribute__((address_space(3)))
; template <int EPI>
; __device__ __forceinline__ int* moe_phase(const Params& p, LAS3 char* lds, int wid, int* pend_in) {
;     ...
;       if (t0 < 8) { int a = 0; LAS3 int* pq = pre + t0 * 128;
;           for (int s = 0; s <= NSL; ++s) { pq[s] = a;
;               if (s < NSL) { int nv = (s < NS && mtv[t0 + 8 * (s / NCOL)] > 0) ? 1 : 0; const int sc = s - MOE_LAG;
;                   if (EPI == 2 && s < MOE_LAG3 && mtv[t0 + 8 * (s >> 3)] > 0) nv += 1;
;                   if (sc >= 0 && sc < NS) nv += mtv[t0 + 8 * (sc / NCOL)];
;                   a += nv; } } } }
.LBB0_417:
	s_andn2_b64 vcc, exec, s[4:5]
	v_mov_b32_e32 v3, 0
	ds_write_b32 v2, v4
	s_cbranch_vccz .LBB0_424
	s_add_i32 s4, s6, 1
	s_cmp_gt_u32 s4, 14
.LBB0_419:
	s_cmp_lt_u32 s6, 14
	s_cbranch_scc1 .LBB0_412
	s_branch .LBB0_426
.LBB0_420:
	s_and_b32 s7, s2, 24
	v_lshl_add_u32 v4, s7, 2, v1
	ds_read_b32 v4, v4
	s_waitcnt lgkmcnt(0)
	v_cmp_lt_i32_e32 vcc, 0, v4
	s_nop 1
	v_cndmask_b32_e64 v4, 0, 1, vcc
	s_cmp_gt_u32 s6, 14
	s_branch .LBB0_415

; #define LAS3 __attribute__((address_space(3)))
; template <int EPI>
; __device__ __forceinline__ int* moe_phase(const Params& p, LAS3 char* lds, int wid, int* pend_in) {
;     ...
;       if (t0 < 8) { int a = 0; LAS3 int* pq = pre + t0 * 128;
;           for (int s = 0; s <= NSL; ++s) { pq[s] = a;
;               if (s < NSL) { int nv = (s < NS && mtv[t0 + 8 * (s / NCOL)] > 0) ? 1 : 0; const int sc = s - MOE_LAG;
;                   if (EPI == 2 && s < MOE_LAG3 && mtv[t0 + 8 * (s >> 3)] > 0) nv += 1;
;                   if (sc >= 0 && sc < NS) nv += mtv[t0 + 8 * (sc / NCOL)];
;                   a += nv; } } } }
.LBB0_424:
	s_and_b32 s4, s2, 24
	v_lshl_add_u32 v3, s4, 2, v1
	ds_read_b32 v3, v3
	s_waitcnt lgkmcnt(0)
	v_cmp_lt_i32_e32 vcc, 0, v3
	s_nop 1
	v_cndmask_b32_e64 v3, 0, 1, vcc
	s_add_i32 s4, s6, 1
	s_cmp_gt_u32 s4, 14
	s_branch .LBB0_419

; template <int EPI>
; __device__ __forceinline__ int* moe_phase(const Params& p, LAS3 char* lds, int wid, int* pend_in) {
;     ...
;             const bool hasP = (s < NS) && (__builtin_amdgcn_readfirstlane(mtv[qq + 8 * ((s < NS) ? s / NCOL : 0)]) > 0);
;             const bool conv = hasP && j == 0;
;             const bool hasX = (EPI == 2) && (s < MOE_LAG3) && (__builtin_amdgcn_readfirstlane(mtv[qq + 8 * ((s < MOE_LAG3) ? (s >> 3) : 0)]) > 0);
;             const bool xconv = hasX && j == (hasP ? 1 : 0);
;             const int k = conv ? 0 : j - (hasP ? 1 : 0) - (hasX ? 1 : 0);
.LBB0_448:
	s_cmp_gt_u32 s12, 14
	s_branch .LBB0_450
	s_lshl_b32 s0, s86, 2
	s_and_b32 s1, s12, 8
	s_add_i32 s0, s0, 0
	s_lshl_b32 s1, s1, 2
	s_add_i32 s0, s0, s1
	s_add_i32 s0, s0, 0x21300
	v_mov_b32_e32 v0, s0
	ds_read_b32 v0, v0
	s_waitcnt lgkmcnt(0)
	v_readfirstlane_b32 s0, v0
	s_cmp_gt_i32 s0, 0
	s_cselect_b64 s[0:1], -1, 0

; #define G_WAIT_V(n) asm volatile("s_waitcnt vmcnt(" #n ")" ::: "memory")
; #define G_WAIT_L(n) asm volatile("s_waitcnt lgkmcnt(" #n ")" ::: "memory")
; #define G_BAR do { asm volatile("" ::: "memory"); __builtin_amdgcn_s_barrier(); asm volatile("" ::: "memory"); } while (0)
; #define G_SCHED __builtin_amdgcn_sched_barrier(0)
; #define STG_A(b, h, kt) do { const unsigned char* _g = A + (size_t)KT_(kt) * ASTEP; \
;         dma16((const void*)(_g + (size_t)((h) * 128) * ROWB), ROWB ? aoff[0][0] : aoff[h][0], lds_u + SA_(b, h) + dma0); \
;         dma16((const void*)(_g + (size_t)((h) * 128 + 64) * ROWB), ROWB ? aoff[0][0] : aoff[h][1], lds_u + SA_(b, h) + dma1); } while (0)
; #define STG_B(b, h, kt) do { const unsigned char* _g = img + (size_t)KT_(kt) * 32768 + (h) * 16384; \
;         dma16((const void*)(_g + dma0), boffl, lds_u + SB_(b, h) + dma0); \
;         dma16((const void*)(_g + dma1), boffl, lds_u + SB_(b, h) + dma1); } while (0)
; #define LDA_(dst, b, h) do { _Pragma("unroll") for (int _m = 0; _m < 4; ++_m) { \
;         dst[_m].lo = *(LAS3 const i32x4d*)(ap0 + SA_(b, h) + _m * 2048); \
;         dst[_m].hi = *(LAS3 const i32x4d*)(ap1 + SA_(b, h) + _m * 2048); } } while (0)
;     ...
;     for (int t = 0; t < nt; t += 2) {
;         const int t1 = (t + 1 < nt) ? t + 1 : nt - 1, t2 = (t + 2 < nt) ? t + 2 : nt - 1, t3 = (t + 3 < nt) ? t + 3 : nt - 1;
;         LDBF(B0, 0, 0); G_SCHED; LDA_(At, 0, 0); STG_A(1, 1, t1);
;         G_WAIT_L(8); G_BAR; G_WAIT_L(0); MMAD(0, 0, At, B0); G_BAR; G_SCHED;
;         LDBF(B1, 0, 1); STG_B(0, 0, t2);
;         G_BAR; G_WAIT_L(0); MMAD(0, 1, At, B1); G_BAR;
;         LDA_(At, 0, 1); STG_A(0, 0, t2);
;         G_BAR; G_WAIT_L(0); MMAD(1, 0, At, B0); G_BAR; G_SCHED;
;         STG_B(0, 1, t2);
;         G_WAIT_V(6); G_BAR; MMAD(1, 1, At, B1); G_BAR;
;         LDBF(B0, 1, 0); G_SCHED; LDA_(At, 1, 0); STG_A(0, 1, t2);
;         G_WAIT_L(8); G_BAR; G_WAIT_L(0); MMAD(0, 0, At, B0); G_BAR; G_SCHED;
;         LDBF(B1, 1, 1); STG_B(1, 0, t3);
;         G_BAR; G_WAIT_L(0); MMAD(0, 1, At, B1); G_BAR;
;         LDA_(At, 1, 1); STG_A(1, 0, t3);
;         G_BAR; G_WAIT_L(0); MMAD(1, 0, At, B0); G_BAR; G_SCHED;
;         STG_B(1, 1, t3);
;         G_WAIT_V(6); G_BAR; MMAD(1, 1, At, B1); G_BAR;
.LBB0_470:
	s_add_i32 s25, vcc_hi, 2
	s_min_u32 s28, vcc_hi, 12
	s_add_u32 s68, s0, 0x80
	s_addc_u32 s69, s1, 0
	s_and_b32 s29, s25, 14
	s_cmp_lt_u32 vcc_hi, 14
	s_cselect_b32 s29, s29, 15
	s_lshl_b32 s30, s29, 15
	s_add_u32 s30, s4, s30
	s_addc_u32 s31, vcc_lo, 0
	s_add_u32 s70, s30, s91
	s_addc_u32 s71, s31, s93
	s_add_u32 s72, s30, s92
	s_addc_u32 s73, s31, s96
	s_lshl_b32 s29, s29, 7
	s_add_u32 s56, s62, s29
	s_addc_u32 s57, s63, 0
	s_add_u32 s29, s30, 0x4000
	s_addc_u32 s30, s31, 0
	s_add_u32 s58, s29, s91
	s_addc_u32 s59, s30, s93
	s_add_u32 s60, s29, s92
	s_addc_u32 s61, s30, s96
	s_add_i32 s28, s28, 3
	s_lshl_b32 s29, s28, 15
	s_add_u32 s29, s4, s29
	s_addc_u32 s30, vcc_lo, 0
	s_add_u32 s36, s29, s91
	s_addc_u32 s37, s30, s93
	s_add_u32 s54, s29, s92
	s_addc_u32 s55, s30, s96
	s_lshl_b32 s28, s28, 7
	s_add_u32 s34, s62, s28
	s_addc_u32 s35, s63, 0
	s_add_u32 s31, s29, 0x4000
	ds_read_b128 v[0:3], v157
	ds_read_b128 v[8:11], v157 offset:8192
	ds_read_b128 v[4:7], v158
	ds_read_b128 v[12:15], v158 offset:8192
	s_addc_u32 s74, s30, 0
	s_add_u32 s28, s31, s91
	s_addc_u32 s29, s74, s93
	s_add_u32 s30, s31, s92
	s_addc_u32 s31, s74, s96
	s_add_u32 s0, s0, 0x100
	s_addc_u32 s1, s1, 0
	s_cmp_gt_u32 vcc_hi, 13
	ds_read_b128 v[160:163], v155
	ds_read_b128 v[168:171], v155 offset:2048
	ds_read_b128 v[164:167], v156
	ds_read_b128 v[172:175], v156 offset:2048
	ds_read_b128 v[176:179], v155 offset:4096
	ds_read_b128 v[184:187], v155 offset:6144
	ds_read_b128 v[180:183], v156 offset:4096
	ds_read_b128 v[188:191], v156 offset:6144
	s_mov_b32 s74, m0
	s_mov_b32 m0, s38
	s_nop 2
	global_load_lds_dwordx4 v153, s[68:69]
	s_mov_b32 m0, s74
	s_nop 0
	s_mov_b32 s74, m0
	s_mov_b32 m0, s39
	s_nop 2
	global_load_lds_dwordx4 v154, s[68:69]
	s_mov_b32 m0, s74
	s_waitcnt lgkmcnt(8)
	s_waitcnt vmcnt(10)
	s_barrier
	s_waitcnt lgkmcnt(0)
	v_readlane_b32 s69, v255, 8
	s_setprio 1
	s_waitcnt lgkmcnt(5)
	v_mfma_scale_f32_16x16x128_f8f6f4 v[140:143], v[0:7], v[160:167], v[140:143], v147, v147 op_sel:[0,1,0] op_sel_hi:[0,0,0]
	v_mfma_scale_f32_16x16x128_f8f6f4 v[132:135], v[8:15], v[160:167], v[132:135], v147, v147 op_sel:[0,1,0] op_sel_hi:[0,0,0]
	s_waitcnt lgkmcnt(4)
	v_mfma_scale_f32_16x16x128_f8f6f4 v[124:127], v[0:7], v[168:175], v[124:127], v147, v147 op_sel:[0,1,0] op_sel_hi:[0,0,0]
	v_mfma_scale_f32_16x16x128_f8f6f4 v[116:119], v[8:15], v[168:175], v[116:119], v147, v147 op_sel:[0,1,0] op_sel_hi:[0,0,0]
	s_waitcnt lgkmcnt(1)
	v_mfma_scale_f32_16x16x128_f8f6f4 v[208:211], v[0:7], v[176:183], v[108:111], v147, v147 op_sel:[0,1,0] op_sel_hi:[0,0,0]
	v_mfma_scale_f32_16x16x128_f8f6f4 v[212:215], v[8:15], v[176:183], v[100:103], v147, v147 op_sel:[0,1,0] op_sel_hi:[0,0,0]
	s_waitcnt lgkmcnt(0)
	v_mfma_scale_f32_16x16x128_f8f6f4 v[216:219], v[0:7], v[184:191], v[92:95], v147, v147 op_sel:[0,1,0] op_sel_hi:[0,0,0]
	v_mfma_scale_f32_16x16x128_f8f6f4 v[220:223], v[8:15], v[184:191], v[84:87], v147, v147 op_sel:[0,1,0] op_sel_hi:[0,0,0]
	s_setprio 0
	s_barrier
	ds_read_b128 v[192:195], v157 offset:16384
	ds_read_b128 v[200:203], v157 offset:24576
	ds_read_b128 v[196:199], v158 offset:16384
	ds_read_b128 v[204:207], v158 offset:24576
	s_mov_b32 s68, m0
	s_mov_b32 m0, s78
	s_nop 2
	global_load_lds_dwordx4 v159, s[70:71]
	s_mov_b32 m0, s68
	v_readlane_b32 s71, v255, 9
	s_mov_b32 s68, m0
	s_mov_b32 m0, s69
	s_nop 2
	global_load_lds_dwordx4 v159, s[72:73]
	s_mov_b32 m0, s68
	s_waitcnt vmcnt(10)
	s_barrier
	s_waitcnt lgkmcnt(0)
	s_setprio 1
	s_waitcnt lgkmcnt(1)
	v_mfma_scale_f32_16x16x128_f8f6f4 v[136:139], v[192:199], v[160:167], v[136:139], v147, v147 op_sel:[0,1,0] op_sel_hi:[0,0,0]
	s_waitcnt lgkmcnt(0)
	v_mfma_scale_f32_16x16x128_f8f6f4 v[128:131], v[200:207], v[160:167], v[128:131], v147, v147 op_sel:[0,1,0] op_sel_hi:[0,0,0]
	v_mfma_scale_f32_16x16x128_f8f6f4 v[120:123], v[192:199], v[168:175], v[120:123], v147, v147 op_sel:[0,1,0] op_sel_hi:[0,0,0]
	v_mfma_scale_f32_16x16x128_f8f6f4 v[112:115], v[200:207], v[168:175], v[112:115], v147, v147 op_sel:[0,1,0] op_sel_hi:[0,0,0]
	v_mfma_scale_f32_16x16x128_f8f6f4 v[224:227], v[192:199], v[176:183], v[104:107], v147, v147 op_sel:[0,1,0] op_sel_hi:[0,0,0]
	v_mfma_scale_f32_16x16x128_f8f6f4 v[176:179], v[200:207], v[176:183], v[96:99], v147, v147 op_sel:[0,1,0] op_sel_hi:[0,0,0]
	v_mfma_scale_f32_16x16x128_f8f6f4 v[180:183], v[192:199], v[184:191], v[88:91], v147, v147 op_sel:[0,1,0] op_sel_hi:[0,0,0]
	v_mfma_scale_f32_16x16x128_f8f6f4 v[184:187], v[200:207], v[184:191], v[20:23], v147, v147 op_sel:[0,1,0] op_sel_hi:[0,0,0]
	s_setprio 0
	s_barrier
	ds_read_b128 v[80:83], v155 offset:16384
	s_nop 2
	ds_read_b128 v[88:91], v155 offset:18432
	ds_read_b128 v[84:87], v156 offset:16384
	ds_read_b128 v[92:95], v156 offset:18432
	ds_read_b128 v[96:99], v155 offset:20480
	ds_read_b128 v[104:107], v155 offset:22528
	ds_read_b128 v[100:103], v156 offset:20480
	ds_read_b128 v[108:111], v156 offset:22528
	s_mov_b32 s68, m0
	s_mov_b32 m0, s94
	s_nop 2
	global_load_lds_dwordx4 v144, s[56:57]
	s_mov_b32 m0, s68
	s_nop 0
	s_mov_b32 s68, m0
	s_mov_b32 m0, s83
	s_nop 2
	global_load_lds_dwordx4 v152, s[56:57]
	s_mov_b32 m0, s68
	s_barrier
; #define G_WAIT_V(n) asm volatile("s_waitcnt vmcnt(" #n ")" ::: "memory")
; #define G_WAIT_L(n) asm volatile("s_waitcnt lgkmcnt(" #n ")" ::: "memory")
; #define G_BAR do { asm volatile("" ::: "memory"); __builtin_amdgcn_s_barrier(); asm volatile("" ::: "memory"); } while (0)
; #define G_SCHED __builtin_amdgcn_sched_barrier(0)
; #define STG_A(b, h, kt) do { const unsigned char* _g = A + (size_t)KT_(kt) * ASTEP; \
;         dma16((const void*)(_g + (size_t)((h) * 128) * ROWB), ROWB ? aoff[0][0] : aoff[h][0], lds_u + SA_(b, h) + dma0); \
;         dma16((const void*)(_g + (size_t)((h) * 128 + 64) * ROWB), ROWB ? aoff[0][0] : aoff[h][1], lds_u + SA_(b, h) + dma1); } while (0)
; #define STG_B(b, h, kt) do { const unsigned char* _g = img + (size_t)KT_(kt) * 32768 + (h) * 16384; \
;         dma16((const void*)(_g + dma0), boffl, lds_u + SB_(b, h) + dma0); \
;         dma16((const void*)(_g + dma1), boffl, lds_u + SB_(b, h) + dma1); } while (0)
; #define LDA_(dst, b, h) do { _Pragma("unroll") for (int _m = 0; _m < 4; ++_m) { \
;         dst[_m].lo = *(LAS3 const i32x4d*)(ap0 + SA_(b, h) + _m * 2048); \
;         dst[_m].hi = *(LAS3 const i32x4d*)(ap1 + SA_(b, h) + _m * 2048); } } while (0)
; #define LDBF(dst, b, h) do { _Pragma("unroll") for (int _n = 0; _n < 2; ++_n) { \
;         dst[_n].lo = *(LAS3 const i32x4d*)(bp0 + (SB_(b, h) - 4 * GHTB) + _n * 8192); \
;         dst[_n].hi = *(LAS3 const i32x4d*)(bp1 + (SB_(b, h) - 4 * GHTB) + _n * 8192); } } while (0)
;     ...
;         G_WAIT_L(8); G_BAR; G_WAIT_L(0); MMAD(0, 0, At, B0); G_BAR; G_SCHED;
;         LDBF(B1, 0, 1); STG_B(0, 0, t2);
;         G_BAR; G_WAIT_L(0); MMAD(0, 1, At, B1); G_BAR;
;         LDA_(At, 0, 1); STG_A(0, 0, t2);
;         G_BAR; G_WAIT_L(0); MMAD(1, 0, At, B0); G_BAR; G_SCHED;
;         STG_B(0, 1, t2);
;         G_WAIT_V(6); G_BAR; MMAD(1, 1, At, B1); G_BAR;
;         LDBF(B0, 1, 0); G_SCHED; LDA_(At, 1, 0); STG_A(0, 1, t2);
	s_waitcnt lgkmcnt(0)
	s_setprio 1
	s_waitcnt lgkmcnt(5)
	v_mfma_scale_f32_16x16x128_f8f6f4 v[76:79], v[0:7], v[80:87], v[76:79], v147, v147 op_sel:[0,1,0] op_sel_hi:[0,0,0]
	v_mfma_scale_f32_16x16x128_f8f6f4 v[68:71], v[8:15], v[80:87], v[68:71], v147, v147 op_sel:[0,1,0] op_sel_hi:[0,0,0]
	s_waitcnt lgkmcnt(4)
	v_mfma_scale_f32_16x16x128_f8f6f4 v[60:63], v[0:7], v[88:95], v[60:63], v147, v147 op_sel:[0,1,0] op_sel_hi:[0,0,0]
	v_mfma_scale_f32_16x16x128_f8f6f4 v[52:55], v[8:15], v[88:95], v[52:55], v147, v147 op_sel:[0,1,0] op_sel_hi:[0,0,0]
	s_waitcnt lgkmcnt(0)
	v_mfma_scale_f32_16x16x128_f8f6f4 v[240:243], v[8:15], v[104:111], v[240:243], v147, v147 op_sel:[0,1,0] op_sel_hi:[0,0,0]
	v_mfma_scale_f32_16x16x128_f8f6f4 v[228:231], v[0:7], v[96:103], v[44:47], v147, v147 op_sel:[0,1,0] op_sel_hi:[0,0,0]
	v_mfma_scale_f32_16x16x128_f8f6f4 v[232:235], v[8:15], v[96:103], v[36:39], v147, v147 op_sel:[0,1,0] op_sel_hi:[0,0,0]
	v_mfma_scale_f32_16x16x128_f8f6f4 v[236:239], v[0:7], v[104:111], v[28:31], v147, v147 op_sel:[0,1,0] op_sel_hi:[0,0,0]
	s_setprio 0
	s_barrier
	s_mov_b32 s68, m0
	s_mov_b32 m0, s82
	s_nop 2
	global_load_lds_dwordx4 v159, s[58:59]
	s_mov_b32 m0, s68
	s_mov_b32 s58, m0
	s_mov_b32 m0, s71
	s_nop 2
	global_load_lds_dwordx4 v159, s[60:61]
	s_mov_b32 m0, s58
	s_waitcnt vmcnt(10)
	s_barrier
	v_readlane_b32 s68, v255, 11
	v_readlane_b32 s60, v255, 10
	s_setprio 1
	v_mfma_scale_f32_16x16x128_f8f6f4 v[72:75], v[192:199], v[80:87], v[72:75], v147, v147 op_sel:[0,1,0] op_sel_hi:[0,0,0]
	v_mfma_scale_f32_16x16x128_f8f6f4 v[64:67], v[200:207], v[80:87], v[64:67], v147, v147 op_sel:[0,1,0] op_sel_hi:[0,0,0]
	v_mfma_scale_f32_16x16x128_f8f6f4 v[56:59], v[192:199], v[88:95], v[56:59], v147, v147 op_sel:[0,1,0] op_sel_hi:[0,0,0]
	v_mfma_scale_f32_16x16x128_f8f6f4 v[48:51], v[200:207], v[88:95], v[48:51], v147, v147 op_sel:[0,1,0] op_sel_hi:[0,0,0]
	v_mfma_scale_f32_16x16x128_f8f6f4 v[244:247], v[192:199], v[96:103], v[40:43], v147, v147 op_sel:[0,1,0] op_sel_hi:[0,0,0]
	v_mfma_scale_f32_16x16x128_f8f6f4 v[248:251], v[200:207], v[96:103], v[32:35], v147, v147 op_sel:[0,1,0] op_sel_hi:[0,0,0]
	v_mfma_scale_f32_16x16x128_f8f6f4 v[148:151], v[192:199], v[104:111], v[24:27], v147, v147 op_sel:[0,1,0] op_sel_hi:[0,0,0]
	v_mfma_scale_f32_16x16x128_f8f6f4 v[80:83], v[200:207], v[104:111], v[16:19], v147, v147 op_sel:[0,1,0] op_sel_hi:[0,0,0]
	s_setprio 0
	s_barrier
	ds_read_b128 v[0:3], v157 offset:32768
	ds_read_b128 v[8:11], v157 offset:40960
	ds_read_b128 v[4:7], v158 offset:32768
	ds_read_b128 v[12:15], v158 offset:40960
	s_nop 0
	ds_read_b128 v[16:19], v155 offset:32768
	ds_read_b128 v[24:27], v155 offset:34816
	ds_read_b128 v[20:23], v156 offset:32768
	ds_read_b128 v[28:31], v156 offset:34816
	ds_read_b128 v[32:35], v155 offset:36864
	ds_read_b128 v[40:43], v155 offset:38912
	ds_read_b128 v[36:39], v156 offset:36864
	ds_read_b128 v[44:47], v156 offset:38912
	s_mov_b32 s58, m0
	s_mov_b32 m0, s79
	s_nop 2
	global_load_lds_dwordx4 v153, s[56:57]
	s_mov_b32 m0, s58
	s_nop 0
	s_mov_b32 s58, m0
	s_mov_b32 m0, s89
	s_nop 2
	global_load_lds_dwordx4 v154, s[56:57]
	s_mov_b32 m0, s58
	s_waitcnt lgkmcnt(8)
	s_waitcnt vmcnt(10)
	s_barrier
	s_waitcnt lgkmcnt(0)
	s_setprio 1
	s_waitcnt lgkmcnt(5)
	v_mfma_scale_f32_16x16x128_f8f6f4 v[140:143], v[0:7], v[16:23], v[140:143], v147, v147 op_sel:[0,1,0] op_sel_hi:[0,0,0]
	v_mfma_scale_f32_16x16x128_f8f6f4 v[132:135], v[8:15], v[16:23], v[132:135], v147, v147 op_sel:[0,1,0] op_sel_hi:[0,0,0]
	s_waitcnt lgkmcnt(4)
	v_mfma_scale_f32_16x16x128_f8f6f4 v[124:127], v[0:7], v[24:31], v[124:127], v147, v147 op_sel:[0,1,0] op_sel_hi:[0,0,0]
	v_mfma_scale_f32_16x16x128_f8f6f4 v[116:119], v[8:15], v[24:31], v[116:119], v147, v147 op_sel:[0,1,0] op_sel_hi:[0,0,0]
	s_waitcnt lgkmcnt(1)
	v_mfma_scale_f32_16x16x128_f8f6f4 v[108:111], v[0:7], v[32:39], v[208:211], v147, v147 op_sel:[0,1,0] op_sel_hi:[0,0,0]
	v_mfma_scale_f32_16x16x128_f8f6f4 v[100:103], v[8:15], v[32:39], v[212:215], v147, v147 op_sel:[0,1,0] op_sel_hi:[0,0,0]
	s_waitcnt lgkmcnt(0)
	v_mfma_scale_f32_16x16x128_f8f6f4 v[92:95], v[0:7], v[40:47], v[216:219], v147, v147 op_sel:[0,1,0] op_sel_hi:[0,0,0]
	v_mfma_scale_f32_16x16x128_f8f6f4 v[84:87], v[8:15], v[40:47], v[220:223], v147, v147 op_sel:[0,1,0] op_sel_hi:[0,0,0]
	s_setprio 0
	s_barrier
	ds_read_b128 v[160:163], v157 offset:49152
	ds_read_b128 v[168:171], v157 offset:57344
	ds_read_b128 v[164:167], v158 offset:49152
	ds_read_b128 v[172:175], v158 offset:57344
	s_mov_b32 s56, m0
	s_mov_b32 m0, s60
	s_nop 2
	global_load_lds_dwordx4 v159, s[36:37]
	s_mov_b32 m0, s56
	s_mov_b32 s36, m0
	s_mov_b32 m0, s68
	s_nop 2
	global_load_lds_dwordx4 v159, s[54:55]
	s_mov_b32 m0, s36
	s_waitcnt vmcnt(10)
	s_barrier
; #define G_WAIT_V(n) asm volatile("s_waitcnt vmcnt(" #n ")" ::: "memory")
; #define G_WAIT_L(n) asm volatile("s_waitcnt lgkmcnt(" #n ")" ::: "memory")
; #define G_BAR do { asm volatile("" ::: "memory"); __builtin_amdgcn_s_barrier(); asm volatile("" ::: "memory"); } while (0)
; #define G_SCHED __builtin_amdgcn_sched_barrier(0)
; #define STG_A(b, h, kt) do { const unsigned char* _g = A + (size_t)KT_(kt) * ASTEP; \
;         dma16((const void*)(_g + (size_t)((h) * 128) * ROWB), ROWB ? aoff[0][0] : aoff[h][0], lds_u + SA_(b, h) + dma0); \
;         dma16((const void*)(_g + (size_t)((h) * 128 + 64) * ROWB), ROWB ? aoff[0][0] : aoff[h][1], lds_u + SA_(b, h) + dma1); } while (0)
; #define STG_B(b, h, kt) do { const unsigned char* _g = img + (size_t)KT_(kt) * 32768 + (h) * 16384; \
;         dma16((const void*)(_g + dma0), boffl, lds_u + SB_(b, h) + dma0); \
;         dma16((const void*)(_g + dma1), boffl, lds_u + SB_(b, h) + dma1); } while (0)
; #define LDA_(dst, b, h) do { _Pragma("unroll") for (int _m = 0; _m < 4; ++_m) { \
;         dst[_m].lo = *(LAS3 const i32x4d*)(ap0 + SA_(b, h) + _m * 2048); \
;         dst[_m].hi = *(LAS3 const i32x4d*)(ap1 + SA_(b, h) + _m * 2048); } } while (0)
; #define LDBF(dst, b, h) do { _Pragma("unroll") for (int _n = 0; _n < 2; ++_n) { \
;         dst[_n].lo = *(LAS3 const i32x4d*)(bp0 + (SB_(b, h) - 4 * GHTB) + _n * 8192); \
;         dst[_n].hi = *(LAS3 const i32x4d*)(bp1 + (SB_(b, h) - 4 * GHTB) + _n * 8192); } } while (0)
;     ...
;         LDBF(B0, 1, 0); G_SCHED; LDA_(At, 1, 0); STG_A(0, 1, t2);
;         G_WAIT_L(8); G_BAR; G_WAIT_L(0); MMAD(0, 0, At, B0); G_BAR; G_SCHED;
;         LDBF(B1, 1, 1); STG_B(1, 0, t3);
;         G_BAR; G_WAIT_L(0); MMAD(0, 1, At, B1); G_BAR;
;         LDA_(At, 1, 1); STG_A(1, 0, t3);
;         G_BAR; G_WAIT_L(0); MMAD(1, 0, At, B0); G_BAR; G_SCHED;
;         STG_B(1, 1, t3);
;         G_WAIT_V(6); G_BAR; MMAD(1, 1, At, B1); G_BAR;
;     }
;     G_WAIT_V(0); G_WAIT_L(0);
	s_waitcnt lgkmcnt(0)
	s_setprio 1
	s_waitcnt lgkmcnt(1)
	v_mfma_scale_f32_16x16x128_f8f6f4 v[136:139], v[160:167], v[16:23], v[136:139], v147, v147 op_sel:[0,1,0] op_sel_hi:[0,0,0]
	s_waitcnt lgkmcnt(0)
	v_mfma_scale_f32_16x16x128_f8f6f4 v[128:131], v[168:175], v[16:23], v[128:131], v147, v147 op_sel:[0,1,0] op_sel_hi:[0,0,0]
	v_mfma_scale_f32_16x16x128_f8f6f4 v[120:123], v[160:167], v[24:31], v[120:123], v147, v147 op_sel:[0,1,0] op_sel_hi:[0,0,0]
	v_mfma_scale_f32_16x16x128_f8f6f4 v[112:115], v[168:175], v[24:31], v[112:115], v147, v147 op_sel:[0,1,0] op_sel_hi:[0,0,0]
	v_mfma_scale_f32_16x16x128_f8f6f4 v[104:107], v[160:167], v[32:39], v[224:227], v147, v147 op_sel:[0,1,0] op_sel_hi:[0,0,0]
	v_mfma_scale_f32_16x16x128_f8f6f4 v[96:99], v[168:175], v[32:39], v[176:179], v147, v147 op_sel:[0,1,0] op_sel_hi:[0,0,0]
	v_mfma_scale_f32_16x16x128_f8f6f4 v[88:91], v[160:167], v[40:47], v[180:183], v147, v147 op_sel:[0,1,0] op_sel_hi:[0,0,0]
	v_mfma_scale_f32_16x16x128_f8f6f4 v[20:23], v[168:175], v[40:47], v[184:187], v147, v147 op_sel:[0,1,0] op_sel_hi:[0,0,0]
	s_setprio 0
	s_barrier
	s_nop 2
	ds_read_b128 v[176:179], v155 offset:49152
	s_nop 0
	ds_read_b128 v[184:187], v155 offset:51200
	ds_read_b128 v[180:183], v156 offset:49152
	ds_read_b128 v[188:191], v156 offset:51200
	ds_read_b128 v[192:195], v155 offset:53248
	ds_read_b128 v[200:203], v155 offset:55296
	ds_read_b128 v[196:199], v156 offset:53248
	ds_read_b128 v[204:207], v156 offset:55296
	s_mov_b32 s36, m0
	s_mov_b32 m0, s90
	s_nop 2
	global_load_lds_dwordx4 v144, s[34:35]
	s_mov_b32 m0, s36
	s_nop 0
	s_mov_b32 s36, m0
	s_mov_b32 m0, s88
	s_nop 2
	global_load_lds_dwordx4 v152, s[34:35]
	s_mov_b32 m0, s36
	s_barrier
	s_waitcnt lgkmcnt(0)
	s_setprio 1
	s_waitcnt lgkmcnt(5)
	v_mfma_scale_f32_16x16x128_f8f6f4 v[76:79], v[0:7], v[176:183], v[76:79], v147, v147 op_sel:[0,1,0] op_sel_hi:[0,0,0]
	v_mfma_scale_f32_16x16x128_f8f6f4 v[68:71], v[8:15], v[176:183], v[68:71], v147, v147 op_sel:[0,1,0] op_sel_hi:[0,0,0]
	s_waitcnt lgkmcnt(4)
	v_mfma_scale_f32_16x16x128_f8f6f4 v[60:63], v[0:7], v[184:191], v[60:63], v147, v147 op_sel:[0,1,0] op_sel_hi:[0,0,0]
	v_mfma_scale_f32_16x16x128_f8f6f4 v[52:55], v[8:15], v[184:191], v[52:55], v147, v147 op_sel:[0,1,0] op_sel_hi:[0,0,0]
	s_waitcnt lgkmcnt(1)
	v_mfma_scale_f32_16x16x128_f8f6f4 v[44:47], v[0:7], v[192:199], v[228:231], v147, v147 op_sel:[0,1,0] op_sel_hi:[0,0,0]
	v_mfma_scale_f32_16x16x128_f8f6f4 v[36:39], v[8:15], v[192:199], v[232:235], v147, v147 op_sel:[0,1,0] op_sel_hi:[0,0,0]
	s_waitcnt lgkmcnt(0)
	v_mfma_scale_f32_16x16x128_f8f6f4 v[28:31], v[0:7], v[200:207], v[236:239], v147, v147 op_sel:[0,1,0] op_sel_hi:[0,0,0]
	v_mfma_scale_f32_16x16x128_f8f6f4 v[240:243], v[8:15], v[200:207], v[240:243], v147, v147 op_sel:[0,1,0] op_sel_hi:[0,0,0]
	s_setprio 0
	s_barrier
	s_mov_b32 s34, m0
	s_mov_b32 m0, s33
	s_nop 2
	global_load_lds_dwordx4 v159, s[28:29]
	s_mov_b32 m0, s34
	s_mov_b32 s28, m0
	s_mov_b32 m0, s6
	s_nop 2
	global_load_lds_dwordx4 v159, s[30:31]
	s_mov_b32 m0, s28
	s_waitcnt vmcnt(10)
	s_barrier
	s_setprio 1
	v_mfma_scale_f32_16x16x128_f8f6f4 v[72:75], v[160:167], v[176:183], v[72:75], v147, v147 op_sel:[0,1,0] op_sel_hi:[0,0,0]
	v_mfma_scale_f32_16x16x128_f8f6f4 v[64:67], v[168:175], v[176:183], v[64:67], v147, v147 op_sel:[0,1,0] op_sel_hi:[0,0,0]
	v_mfma_scale_f32_16x16x128_f8f6f4 v[56:59], v[160:167], v[184:191], v[56:59], v147, v147 op_sel:[0,1,0] op_sel_hi:[0,0,0]
	v_mfma_scale_f32_16x16x128_f8f6f4 v[48:51], v[168:175], v[184:191], v[48:51], v147, v147 op_sel:[0,1,0] op_sel_hi:[0,0,0]
	v_mfma_scale_f32_16x16x128_f8f6f4 v[40:43], v[160:167], v[192:199], v[244:247], v147, v147 op_sel:[0,1,0] op_sel_hi:[0,0,0]
	v_mfma_scale_f32_16x16x128_f8f6f4 v[32:35], v[168:175], v[192:199], v[248:251], v147, v147 op_sel:[0,1,0] op_sel_hi:[0,0,0]
	v_mfma_scale_f32_16x16x128_f8f6f4 v[24:27], v[160:167], v[200:207], v[148:151], v147, v147 op_sel:[0,1,0] op_sel_hi:[0,0,0]
	v_mfma_scale_f32_16x16x128_f8f6f4 v[16:19], v[168:175], v[200:207], v[80:83], v147, v147 op_sel:[0,1,0] op_sel_hi:[0,0,0]
	s_setprio 0
	s_barrier
	s_mov_b32 vcc_hi, s25
	s_cbranch_scc0 .LBB0_470
	s_waitcnt vmcnt(0)
	s_waitcnt lgkmcnt(0)
	s_mov_b32 s0, s77
	s_mov_b32 s70, s82
	s_mov_b32 s72, s83
	s_mov_b32 s59, s89
	s_mov_b32 s61, s79
	s_cmp_eq_u32 s0, 0
	s_cbranch_scc0 .LBB0_473
	s_barrier

; __device__ __forceinline__ int ld_now(const int* ptr) { int r = ld_early(ptr); LD_WAIT(r); return r; }
; template <int EPI>
; __device__ __forceinline__ int* moe_phase(const Params& p, LAS3 char* lds, int wid, int* pend_in) {
;     ...
;                     if (conv) {
;                         const bool have = (EPI == 3) && (__builtin_amdgcn_readfirstlane(ld_now(sy.flag)) != 0);
;                         if (have) { }
;                         else if (EPI == 2) convert_image<2 * DFF>(p.w_gate_up + (size_t)e * D * (2 * DFF), pn * 128, DFF + pn * 128, img, lds, wid);
;                         else convert_image<D>(p.w_down + (size_t)e * DFF * D, pn * 256, pn * 256 + 128, img, lds, wid);
.LBB0_488:
	s_and_b64 vcc, exec, s[28:29]
	v_mov_b64_e32 v[0:1], s[0:1]
	s_mov_b32 s28, 0x34000
	s_mov_b32 s29, 0x38000
	s_cbranch_vccz .LBB0_494
	global_load_dword v0, v150, s[16:17] sc1
	s_waitcnt vmcnt(0)
	v_readfirstlane_b32 s4, v0
	s_cmp_lg_u32 s4, 0
	s_cbranch_scc1 .Lgu_have
	s_lshl_b32 s4, s26, 11
	s_lshl_b64 s[26:27], s[4:5], 14
	s_lshl_b32 s4, s24, 7
	s_add_u32 s0, s73, s26
	v_mbcnt_lo_u32_b32 v66, -1, 0
	v_mbcnt_hi_u32_b32 v66, -1, v66
	s_addc_u32 s1, s74, s27
	s_add_i32 s25, s4, 0x780
	v_mov_b32_e32 v0, s25
	v_mov_b32_e32 v1, s4
	v_cmp_gt_i32_e32 vcc, 32, v66
	v_lshlrev_b32_e32 v67, 2, v66
	v_lshlrev_b32_e32 v68, 9, v66
	v_cndmask_b32_e32 v0, v0, v1, vcc
	v_add_u32_e32 v0, v0, v67
	v_ashrrev_i32_e32 v1, 31, v0
	v_lshlrev_b64 v[64:65], 2, v[0:1]
	v_lshl_add_u64 v[132:133], s[0:1], 0, v[64:65]
	s_waitcnt vmcnt(14)
	v_add_co_u32_e32 v4, vcc, s19, v132
	v_and_b32_e32 v68, 0xffffc000, v68
	s_nop 0
	v_addc_co_u32_e32 v5, vcc, 0, v133, vcc
	s_waitcnt vmcnt(13)
	v_add_co_u32_e32 v8, vcc, s7, v132
	global_load_dwordx4 v[0:3], v[132:133], off nt
	s_nop 0
	global_load_dwordx4 v[4:7], v[4:5], off nt
	v_addc_co_u32_e32 v9, vcc, 0, v133, vcc
	s_waitcnt vmcnt(14)
	v_add_co_u32_e32 v12, vcc, s98, v132
	v_and_b32_e32 v67, 0x7c, v67
	s_nop 0
	v_addc_co_u32_e32 v13, vcc, 0, v133, vcc
	s_waitcnt vmcnt(13)
	v_add_co_u32_e32 v16, vcc, s9, v132
	global_load_dwordx4 v[8:11], v[8:9], off nt
	s_nop 0
	global_load_dwordx4 v[12:15], v[12:13], off nt
	v_addc_co_u32_e32 v17, vcc, 0, v133, vcc
	s_waitcnt vmcnt(14)
	v_add_co_u32_e32 v20, vcc, s3, v132
	v_add_u32_e32 v68, 0, v68
	s_nop 0
	v_addc_co_u32_e32 v21, vcc, 0, v133, vcc
	s_waitcnt vmcnt(13)
	v_add_co_u32_e32 v24, vcc, s18, v132
	global_load_dwordx4 v[16:19], v[16:17], off nt
	s_nop 0
	global_load_dwordx4 v[20:23], v[20:21], off nt
	v_addc_co_u32_e32 v25, vcc, 0, v133, vcc
	s_waitcnt vmcnt(14)
	v_add_co_u32_e32 v28, vcc, s95, v132
	v_lshlrev_b32_e32 v136, 4, v66
	s_nop 0
	v_addc_co_u32_e32 v29, vcc, 0, v133, vcc
	s_waitcnt vmcnt(13)
	v_add_co_u32_e32 v32, vcc, s31, v132
	global_load_dwordx4 v[24:27], v[24:25], off nt
	s_nop 0
	global_load_dwordx4 v[28:31], v[28:29], off nt
	v_addc_co_u32_e32 v33, vcc, 0, v133, vcc
	s_waitcnt vmcnt(14)
	v_add_co_u32_e32 v36, vcc, s34, v132
	v_readlane_b32 s0, v254, 56
	s_nop 0
	v_addc_co_u32_e32 v37, vcc, 0, v133, vcc
	s_waitcnt vmcnt(13)
	v_add_co_u32_e32 v40, vcc, s35, v132
	global_load_dwordx4 v[32:35], v[32:33], off nt
	s_nop 0
	global_load_dwordx4 v[36:39], v[36:37], off nt
	v_addc_co_u32_e32 v41, vcc, 0, v133, vcc
	s_waitcnt vmcnt(14)
	v_add_co_u32_e32 v44, vcc, s54, v132
	v_lshl_add_u32 v69, v67, 7, v68
	s_nop 0
	v_addc_co_u32_e32 v45, vcc, 0, v133, vcc
	s_waitcnt vmcnt(13)
	v_add_co_u32_e32 v48, vcc, s55, v132
	global_load_dwordx4 v[40:43], v[40:41], off nt
	s_nop 0
	global_load_dwordx4 v[44:47], v[44:45], off nt
	v_addc_co_u32_e32 v49, vcc, 0, v133, vcc
	s_waitcnt vmcnt(14)
	v_add_co_u32_e32 v52, vcc, s28, v132
	v_or_b32_e32 v70, 2, v67
	s_nop 0
	v_addc_co_u32_e32 v53, vcc, 0, v133, vcc
	s_waitcnt vmcnt(13)
	v_add_co_u32_e32 v56, vcc, s29, v132
	global_load_dwordx4 v[48:51], v[48:49], off nt
	s_nop 0
	global_load_dwordx4 v[52:55], v[52:53], off nt
	v_addc_co_u32_e32 v57, vcc, 0, v133, vcc
	s_waitcnt vmcnt(14)
	v_add_co_u32_e32 v60, vcc, s30, v132
	v_or_b32_e32 v67, 3, v67
	s_nop 0
	v_addc_co_u32_e32 v61, vcc, 0, v133, vcc
	global_load_dwordx4 v[56:59], v[56:57], off nt
	s_nop 0
	global_load_dwordx4 v[60:63], v[60:61], off nt
	v_add_u32_e32 v137, s0, v136
	v_lshlrev_b32_e32 v66, 1, v66
	v_readlane_b32 s0, v254, 0
	v_lshl_add_u32 v71, v70, 7, v68
	v_lshrrev_b32_e32 v70, 1, v70
	v_lshl_add_u32 v68, v67, 7, v68
	v_lshrrev_b32_e32 v67, 1, v67
	v_bitop3_b32 v66, v66, s0, 6 bitop3:0x6c
	v_bitop3_b32 v70, v70, s0, 7 bitop3:0x6c
	v_bitop3_b32 v67, v67, s0, 7 bitop3:0x6c
	s_lshl_b32 s0, s13, 3
	s_and_b32 s0, s0, 0x180
	s_lshl_b32 s1, s86, 4
	s_add_i32 s0, s0, s1
	s_or_b32 s4, s0, s24
	v_readlane_b32 s36, v254, 20
	s_lshl_b64 s[0:1], s[4:5], 19
	v_readlane_b32 s42, v254, 26
	v_readlane_b32 s43, v254, 27
	s_add_u32 s0, s42, s0
	s_addc_u32 s1, s43, s1
	v_readlane_b32 s4, v255, 0
	s_add_u32 s24, s4, s26
	v_readlane_b32 s4, v255, 2
	v_lshlrev_b32_e32 v66, 4, v66
	v_lshlrev_b32_e32 v70, 4, v70
	v_lshlrev_b32_e32 v67, 4, v67
	s_addc_u32 s25, s4, s27
	v_add_u32_e32 v138, 0x400, v137
	v_add_u32_e32 v139, 0x800, v137
	v_add_u32_e32 v140, 0xc00, v137
	v_lshl_add_u64 v[134:135], s[24:25], 0, v[64:65]
	s_mov_b32 s13, -2
	v_add_u32_e32 v141, v69, v66
	v_add_u32_e32 v142, v71, v70
	v_add_u32_e32 v143, v68, v67
	v_readlane_b32 s37, v254, 21
	v_readlane_b32 s38, v254, 22
	v_readlane_b32 s39, v254, 23
	v_readlane_b32 s40, v254, 24
	v_readlane_b32 s41, v254, 25
	v_readlane_b32 s44, v254, 28
	v_readlane_b32 s45, v254, 29
	v_readlane_b32 s46, v254, 30
	v_readlane_b32 s47, v254, 31
	v_readlane_b32 s48, v254, 32
	v_readlane_b32 s49, v254, 33
	v_readlane_b32 s50, v254, 34
	v_readlane_b32 s51, v254, 35

; __device__ __forceinline__ int lane_id() { int r; asm volatile("v_mbcnt_lo_u32_b32 %0, -1, 0\n\tv_mbcnt_hi_u32_b32 %0, -1, %0" : "=v"(r)); return r; }
; #define LD_WAIT(r) asm volatile("s_waitcnt vmcnt(0)" : "+v"(r) :: "memory")
; template <int EPI>
; __device__ __forceinline__ int* moe_phase(const Params& p, LAS3 char* lds, int wid, int* pend_in) {
;     ...
;                         const int t0 = wid * 64 + lane_id();
;                         if (t0 == 0) { __hip_atomic_store(sy.flag, 1, __ATOMIC_RELAXED, __HIP_MEMORY_SCOPE_AGENT); unsigned c0 = inc_early(&qctr[qq]); LD_WAIT(c0); slot[par ^ 1] = ((unsigned)qq << 20) | c0; }
.Lgu_have:
	s_waitcnt vmcnt(0)
	s_barrier
	s_waitcnt vmcnt(15)
	v_mbcnt_lo_u32_b32 v0, -1, 0
	v_mbcnt_hi_u32_b32 v0, -1, v0
	s_nop 0
	v_sub_u32_e32 v0, 0, v0
	v_cmp_eq_u32_e32 vcc, s75, v0
	s_and_saveexec_b64 s[0:1], vcc
	s_cbranch_execz .LBB0_493
	global_store_dword v150, v145, s[16:17] sc1
	v_readlane_b32 s16, v255, 17
	v_readlane_b32 s17, v255, 18
	v_mov_b32 v0, 0
	v_mov_b32 v1, 1
	s_nop 4
	global_atomic_add v1, v0, v1, s[16:17] sc0
	v_readlane_b32 s4, v255, 19
	s_waitcnt vmcnt(0)
	s_nop 1
	v_or_b32_e32 v0, s4, v1
	v_readlane_b32 s4, v255, 21
	s_nop 1
	v_mov_b32_e32 v1, s4
	ds_write_b32 v1, v0

; #define G_WAIT_V(n) asm volatile("s_waitcnt vmcnt(" #n ")" ::: "memory")
; #define G_WAIT_L(n) asm volatile("s_waitcnt lgkmcnt(" #n ")" ::: "memory")
; #define G_BAR do { asm volatile("" ::: "memory"); __builtin_amdgcn_s_barrier(); asm volatile("" ::: "memory"); } while (0)
; #define G_SCHED __builtin_amdgcn_sched_barrier(0)
; #define STG_A(b, h, kt) do { const unsigned char* _g = A + (size_t)KT_(kt) * ASTEP; \
;         dma16((const void*)(_g + (size_t)((h) * 128) * ROWB), ROWB ? aoff[0][0] : aoff[h][0], lds_u + SA_(b, h) + dma0); \
;         dma16((const void*)(_g + (size_t)((h) * 128 + 64) * ROWB), ROWB ? aoff[0][0] : aoff[h][1], lds_u + SA_(b, h) + dma1); } while (0)
; #define STG_B(b, h, kt) do { const unsigned char* _g = img + (size_t)KT_(kt) * 32768 + (h) * 16384; \
;         dma16((const void*)(_g + dma0), boffl, lds_u + SB_(b, h) + dma0); \
;         dma16((const void*)(_g + dma1), boffl, lds_u + SB_(b, h) + dma1); } while (0)
; #define LDA_(dst, b, h) do { _Pragma("unroll") for (int _m = 0; _m < 4; ++_m) { \
;         dst[_m].lo = *(LAS3 const i32x4d*)(ap0 + SA_(b, h) + _m * 2048); \
;         dst[_m].hi = *(LAS3 const i32x4d*)(ap1 + SA_(b, h) + _m * 2048); } } while (0)
; #define LDBF(dst, b, h) do { _Pragma("unroll") for (int _n = 0; _n < 2; ++_n) { \
;         dst[_n].lo = *(LAS3 const i32x4d*)(bp0 + (SB_(b, h) - 4 * GHTB) + _n * 8192); \
;         dst[_n].hi = *(LAS3 const i32x4d*)(bp1 + (SB_(b, h) - 4 * GHTB) + _n * 8192); } } while (0)
;     ...
;     for (int t = 0; t < nt; t += 2) {
;         const int t1 = (t + 1 < nt) ? t + 1 : nt - 1, t2 = (t + 2 < nt) ? t + 2 : nt - 1, t3 = (t + 3 < nt) ? t + 3 : nt - 1;
;         LDBF(B0, 0, 0); G_SCHED; LDA_(At, 0, 0); STG_A(1, 1, t1);
;         G_WAIT_L(8); G_BAR; G_WAIT_L(0); MMAD(0, 0, At, B0); G_BAR; G_SCHED;
;         LDBF(B1, 0, 1); STG_B(0, 0, t2);
;         G_BAR; G_WAIT_L(0); MMAD(0, 1, At, B1); G_BAR;
;         LDA_(At, 0, 1); STG_A(0, 0, t2);
;         G_BAR; G_WAIT_L(0); MMAD(1, 0, At, B0); G_BAR; G_SCHED;
;         STG_B(0, 1, t2);
;         G_WAIT_V(6); G_BAR; MMAD(1, 1, At, B1); G_BAR;
.LBB0_562:
	s_add_i32 vcc_lo, vcc_hi, 2
	s_add_u32 s30, s64, s0
	s_addc_u32 s31, s65, s1
	s_add_u32 s68, s30, 0xc000
	s_addc_u32 s69, s31, 0
	s_add_u32 s76, s30, 0xe000
	s_addc_u32 s77, s31, 0
	s_add_u32 s0, s0, 0x10000
	s_addc_u32 s1, s1, 0
	s_and_b32 s30, s0, 0x70000
	s_cmp_lt_u32 vcc_hi, 14
	s_cselect_b32 s30, s30, 0x78000
	s_add_u32 s31, s4, s30
	s_addc_u32 s34, s25, 0
	s_add_u32 s84, s31, s91
	s_addc_u32 s85, s34, s93
	s_add_u32 s80, s31, s92
	s_addc_u32 s81, s34, s96
	s_add_u32 s74, s64, s30
	s_addc_u32 s75, s65, 0
	s_add_u32 s72, s74, 0x2000
	s_addc_u32 s73, s75, 0
	s_add_u32 s30, s31, 0x4000
	s_addc_u32 s31, s34, 0
	s_add_u32 s70, s30, s91
	s_addc_u32 s71, s31, s93
	s_add_u32 s62, s30, s92
	s_addc_u32 s63, s31, s96
	s_add_u32 s60, s74, 0x4000
	s_addc_u32 s61, s75, 0
	s_add_u32 s58, s74, 0x6000
	s_addc_u32 s59, s75, 0
	s_min_u32 s30, vcc_hi, 12
	s_lshl_b32 s30, s30, 15
	s_add_i32 s30, s30, 0x18000
	s_and_b32 s30, s30, 0x78000
	s_add_u32 s31, s4, s30
	s_addc_u32 s34, s25, 0
	s_add_u32 s56, s31, s91
	s_addc_u32 s57, s34, s93
	s_add_u32 s54, s31, s92
	s_addc_u32 s55, s34, s96
	s_add_u32 s48, s64, s30
	s_addc_u32 s49, s65, 0
	s_add_u32 s36, s48, 0x2000
	ds_read_b128 v[0:3], v139
	ds_read_b128 v[148:151], v139 offset:8192
	ds_read_b128 v[4:7], v140
	ds_read_b128 v[152:155], v140 offset:8192
	s_addc_u32 s37, s49, 0
	s_add_u32 s30, s31, 0x4000
	s_addc_u32 s31, s34, 0
	s_add_u32 s34, s30, s91
	s_addc_u32 s35, s31, s93
	s_add_u32 s30, s30, s92
	s_addc_u32 s31, s31, s96
	s_cmp_gt_u32 vcc_hi, 13
	ds_read_b128 v[156:159], v137
	ds_read_b128 v[164:167], v137 offset:2048
	ds_read_b128 v[160:163], v138
	ds_read_b128 v[168:171], v138 offset:2048
	ds_read_b128 v[172:175], v137 offset:4096
	ds_read_b128 v[180:183], v137 offset:6144
	ds_read_b128 v[176:179], v138 offset:4096
	ds_read_b128 v[184:187], v138 offset:6144
	s_mov_b32 s39, s78
	s_mov_b32 s78, m0
	s_mov_b32 m0, s40
	s_nop 2
	global_load_lds_dwordx4 v136, s[68:69]
	s_mov_b32 m0, s78
	s_mov_b32 s68, m0
	s_mov_b32 m0, s41
	s_nop 2
	global_load_lds_dwordx4 v136, s[76:77]
	s_mov_b32 m0, s68
	s_waitcnt lgkmcnt(8)
	s_waitcnt vmcnt(10)
	s_barrier
	s_waitcnt lgkmcnt(0)
	v_readlane_b32 s69, v255, 8
	s_mov_b32 s78, s39
	s_setprio 1
	s_waitcnt lgkmcnt(5)
	v_mfma_scale_f32_16x16x128_f8f6f4 v[132:135], v[0:7], v[156:163], v[132:135], v144, v144 op_sel:[0,1,0] op_sel_hi:[0,0,0]
	s_waitcnt lgkmcnt(4)
	v_mfma_scale_f32_16x16x128_f8f6f4 v[116:119], v[148:155], v[164:171], v[116:119], v144, v144 op_sel:[0,1,0] op_sel_hi:[0,0,0]
	s_waitcnt lgkmcnt(1)
	v_mfma_scale_f32_16x16x128_f8f6f4 v[108:111], v[0:7], v[172:179], v[108:111], v144, v144 op_sel:[0,1,0] op_sel_hi:[0,0,0]
	v_mfma_scale_f32_16x16x128_f8f6f4 v[196:199], v[148:155], v[156:163], v[128:131], v144, v144 op_sel:[0,1,0] op_sel_hi:[0,0,0]
	v_mfma_scale_f32_16x16x128_f8f6f4 v[200:203], v[0:7], v[164:171], v[124:127], v144, v144 op_sel:[0,1,0] op_sel_hi:[0,0,0]
	v_mfma_scale_f32_16x16x128_f8f6f4 v[204:207], v[148:155], v[172:179], v[100:103], v144, v144 op_sel:[0,1,0] op_sel_hi:[0,0,0]
	s_waitcnt lgkmcnt(0)
	v_mfma_scale_f32_16x16x128_f8f6f4 v[208:211], v[0:7], v[180:187], v[92:95], v144, v144 op_sel:[0,1,0] op_sel_hi:[0,0,0]
	v_mfma_scale_f32_16x16x128_f8f6f4 v[212:215], v[148:155], v[180:187], v[84:87], v144, v144 op_sel:[0,1,0] op_sel_hi:[0,0,0]
	s_setprio 0
	s_barrier
	s_nop 0
	ds_read_b128 v[124:127], v139 offset:16384
	ds_read_b128 v[188:191], v139 offset:24576
	ds_read_b128 v[128:131], v140 offset:16384
	ds_read_b128 v[192:195], v140 offset:24576
	s_mov_b32 s68, m0
	s_mov_b32 m0, s39
	s_nop 2
	global_load_lds_dwordx4 v141, s[84:85]
	s_mov_b32 m0, s68
	s_nop 0
	s_mov_b32 s68, m0
	s_mov_b32 m0, s69
	s_nop 2
	global_load_lds_dwordx4 v141, s[80:81]
	s_mov_b32 m0, s68
	s_waitcnt vmcnt(10)
	s_barrier
	s_waitcnt lgkmcnt(0)
	s_setprio 1
	s_waitcnt lgkmcnt(1)
	v_mfma_scale_f32_16x16x128_f8f6f4 v[120:123], v[124:131], v[156:163], v[120:123], v144, v144 op_sel:[0,1,0] op_sel_hi:[0,0,0]
	s_waitcnt lgkmcnt(0)
	v_mfma_scale_f32_16x16x128_f8f6f4 v[112:115], v[188:195], v[156:163], v[112:115], v144, v144 op_sel:[0,1,0] op_sel_hi:[0,0,0]
	v_mfma_scale_f32_16x16x128_f8f6f4 v[104:107], v[124:131], v[164:171], v[104:107], v144, v144 op_sel:[0,1,0] op_sel_hi:[0,0,0]
	v_mfma_scale_f32_16x16x128_f8f6f4 v[164:167], v[188:195], v[164:171], v[96:99], v144, v144 op_sel:[0,1,0] op_sel_hi:[0,0,0]
	v_mfma_scale_f32_16x16x128_f8f6f4 v[168:171], v[124:131], v[172:179], v[88:91], v144, v144 op_sel:[0,1,0] op_sel_hi:[0,0,0]
	v_mfma_scale_f32_16x16x128_f8f6f4 v[172:175], v[188:195], v[172:179], v[80:83], v144, v144 op_sel:[0,1,0] op_sel_hi:[0,0,0]
	v_mfma_scale_f32_16x16x128_f8f6f4 v[176:179], v[124:131], v[180:187], v[76:79], v144, v144 op_sel:[0,1,0] op_sel_hi:[0,0,0]
	v_mfma_scale_f32_16x16x128_f8f6f4 v[180:183], v[188:195], v[180:187], v[72:75], v144, v144 op_sel:[0,1,0] op_sel_hi:[0,0,0]
	s_setprio 0
	s_barrier
	s_nop 4
	ds_read_b128 v[72:75], v137 offset:16384
	ds_read_b128 v[80:83], v137 offset:18432
	ds_read_b128 v[76:79], v138 offset:16384
	ds_read_b128 v[84:87], v138 offset:18432
	ds_read_b128 v[88:91], v137 offset:20480
	ds_read_b128 v[96:99], v137 offset:22528
	ds_read_b128 v[92:95], v138 offset:20480
	ds_read_b128 v[100:103], v138 offset:22528
	s_mov_b32 s68, m0
	s_mov_b32 m0, s94
	s_nop 2
	global_load_lds_dwordx4 v136, s[74:75]
	s_mov_b32 m0, s68
	s_nop 0
	s_mov_b32 s68, m0
	s_mov_b32 m0, s83
	s_nop 2
	global_load_lds_dwordx4 v136, s[72:73]
	s_mov_b32 m0, s68
	s_barrier
; #define G_WAIT_V(n) asm volatile("s_waitcnt vmcnt(" #n ")" ::: "memory")
; #define G_WAIT_L(n) asm volatile("s_waitcnt lgkmcnt(" #n ")" ::: "memory")
; #define G_BAR do { asm volatile("" ::: "memory"); __builtin_amdgcn_s_barrier(); asm volatile("" ::: "memory"); } while (0)
; #define G_SCHED __builtin_amdgcn_sched_barrier(0)
; #define STG_A(b, h, kt) do { const unsigned char* _g = A + (size_t)KT_(kt) * ASTEP; \
;         dma16((const void*)(_g + (size_t)((h) * 128) * ROWB), ROWB ? aoff[0][0] : aoff[h][0], lds_u + SA_(b, h) + dma0); \
;         dma16((const void*)(_g + (size_t)((h) * 128 + 64) * ROWB), ROWB ? aoff[0][0] : aoff[h][1], lds_u + SA_(b, h) + dma1); } while (0)
; #define STG_B(b, h, kt) do { const unsigned char* _g = img + (size_t)KT_(kt) * 32768 + (h) * 16384; \
;         dma16((const void*)(_g + dma0), boffl, lds_u + SB_(b, h) + dma0); \
;         dma16((const void*)(_g + dma1), boffl, lds_u + SB_(b, h) + dma1); } while (0)
; #define LDA_(dst, b, h) do { _Pragma("unroll") for (int _m = 0; _m < 4; ++_m) { \
;         dst[_m].lo = *(LAS3 const i32x4d*)(ap0 + SA_(b, h) + _m * 2048); \
;         dst[_m].hi = *(LAS3 const i32x4d*)(ap1 + SA_(b, h) + _m * 2048); } } while (0)
; #define LDBF(dst, b, h) do { _Pragma("unroll") for (int _n = 0; _n < 2; ++_n) { \
;         dst[_n].lo = *(LAS3 const i32x4d*)(bp0 + (SB_(b, h) - 4 * GHTB) + _n * 8192); \
;         dst[_n].hi = *(LAS3 const i32x4d*)(bp1 + (SB_(b, h) - 4 * GHTB) + _n * 8192); } } while (0)
;     ...
;         STG_B(0, 1, t2);
;         G_WAIT_V(6); G_BAR; MMAD(1, 1, At, B1); G_BAR;
;         LDBF(B0, 1, 0); G_SCHED; LDA_(At, 1, 0); STG_A(0, 1, t2);
;         G_WAIT_L(8); G_BAR; G_WAIT_L(0); MMAD(0, 0, At, B0); G_BAR; G_SCHED;
;         LDBF(B1, 1, 1); STG_B(1, 0, t3);
;         G_BAR; G_WAIT_L(0); MMAD(0, 1, At, B1); G_BAR;
;         LDA_(At, 1, 1); STG_A(1, 0, t3);
;         G_BAR; G_WAIT_L(0); MMAD(1, 0, At, B0); G_BAR; G_SCHED;
	s_waitcnt lgkmcnt(0)
	s_setprio 1
	s_waitcnt lgkmcnt(5)
	v_mfma_scale_f32_16x16x128_f8f6f4 v[68:71], v[0:7], v[72:79], v[68:71], v144, v144 op_sel:[0,1,0] op_sel_hi:[0,0,0]
	v_mfma_scale_f32_16x16x128_f8f6f4 v[64:67], v[148:155], v[72:79], v[64:67], v144, v144 op_sel:[0,1,0] op_sel_hi:[0,0,0]
	s_waitcnt lgkmcnt(4)
	v_mfma_scale_f32_16x16x128_f8f6f4 v[60:63], v[0:7], v[80:87], v[60:63], v144, v144 op_sel:[0,1,0] op_sel_hi:[0,0,0]
	v_mfma_scale_f32_16x16x128_f8f6f4 v[52:55], v[148:155], v[80:87], v[52:55], v144, v144 op_sel:[0,1,0] op_sel_hi:[0,0,0]
	s_waitcnt lgkmcnt(1)
	v_mfma_scale_f32_16x16x128_f8f6f4 v[216:219], v[0:7], v[88:95], v[44:47], v144, v144 op_sel:[0,1,0] op_sel_hi:[0,0,0]
	v_mfma_scale_f32_16x16x128_f8f6f4 v[220:223], v[148:155], v[88:95], v[40:43], v144, v144 op_sel:[0,1,0] op_sel_hi:[0,0,0]
	s_waitcnt lgkmcnt(0)
	v_mfma_scale_f32_16x16x128_f8f6f4 v[224:227], v[0:7], v[96:103], v[28:31], v144, v144 op_sel:[0,1,0] op_sel_hi:[0,0,0]
	v_mfma_scale_f32_16x16x128_f8f6f4 v[228:231], v[148:155], v[96:103], v[24:27], v144, v144 op_sel:[0,1,0] op_sel_hi:[0,0,0]
	s_setprio 0
	s_barrier
	s_mov_b32 s68, m0
	s_mov_b32 m0, s82
	s_nop 2
	global_load_lds_dwordx4 v141, s[70:71]
	s_mov_b32 m0, s68
	v_readlane_b32 s71, v255, 9
	s_mov_b32 s68, m0
	s_mov_b32 m0, s71
	s_nop 2
	global_load_lds_dwordx4 v141, s[62:63]
	s_mov_b32 m0, s68
	s_waitcnt vmcnt(10)
	s_barrier
	v_readlane_b32 s68, v255, 11
	s_setprio 1
	v_mfma_scale_f32_16x16x128_f8f6f4 v[56:59], v[124:131], v[72:79], v[56:59], v144, v144 op_sel:[0,1,0] op_sel_hi:[0,0,0]
	v_mfma_scale_f32_16x16x128_f8f6f4 v[48:51], v[188:195], v[72:79], v[48:51], v144, v144 op_sel:[0,1,0] op_sel_hi:[0,0,0]
	v_mfma_scale_f32_16x16x128_f8f6f4 v[232:235], v[124:131], v[80:87], v[36:39], v144, v144 op_sel:[0,1,0] op_sel_hi:[0,0,0]
	v_mfma_scale_f32_16x16x128_f8f6f4 v[236:239], v[188:195], v[80:87], v[32:35], v144, v144 op_sel:[0,1,0] op_sel_hi:[0,0,0]
	v_mfma_scale_f32_16x16x128_f8f6f4 v[240:243], v[124:131], v[88:95], v[20:23], v144, v144 op_sel:[0,1,0] op_sel_hi:[0,0,0]
	v_mfma_scale_f32_16x16x128_f8f6f4 v[244:247], v[188:195], v[88:95], v[16:19], v144, v144 op_sel:[0,1,0] op_sel_hi:[0,0,0]
	v_mfma_scale_f32_16x16x128_f8f6f4 v[248:251], v[124:131], v[96:103], v[12:15], v144, v144 op_sel:[0,1,0] op_sel_hi:[0,0,0]
	v_mfma_scale_f32_16x16x128_f8f6f4 v[188:191], v[188:195], v[96:103], v[8:11], v144, v144 op_sel:[0,1,0] op_sel_hi:[0,0,0]
	s_setprio 0
	s_barrier
	ds_read_b128 v[0:3], v139 offset:32768
	s_nop 3
	ds_read_b128 v[8:11], v139 offset:40960
	ds_read_b128 v[4:7], v140 offset:32768
	ds_read_b128 v[12:15], v140 offset:40960
	ds_read_b128 v[16:19], v137 offset:32768
	ds_read_b128 v[24:27], v137 offset:34816
	ds_read_b128 v[20:23], v138 offset:32768
	ds_read_b128 v[28:31], v138 offset:34816
	ds_read_b128 v[32:35], v137 offset:36864
	ds_read_b128 v[40:43], v137 offset:38912
	ds_read_b128 v[36:39], v138 offset:36864
	ds_read_b128 v[44:47], v138 offset:38912
	s_mov_b32 s62, m0
	s_mov_b32 m0, s79
	s_nop 2
	global_load_lds_dwordx4 v136, s[60:61]
	s_mov_b32 m0, s62
	s_mov_b32 s60, m0
	s_mov_b32 m0, s89
	s_nop 2
	global_load_lds_dwordx4 v136, s[58:59]
	s_mov_b32 m0, s60
	s_waitcnt lgkmcnt(8)
	s_waitcnt vmcnt(10)
	s_barrier
	s_waitcnt lgkmcnt(0)
	v_readlane_b32 s60, v255, 10
	s_setprio 1
	s_waitcnt lgkmcnt(5)
	v_mfma_scale_f32_16x16x128_f8f6f4 v[132:135], v[0:7], v[16:23], v[132:135], v144, v144 op_sel:[0,1,0] op_sel_hi:[0,0,0]
	v_mfma_scale_f32_16x16x128_f8f6f4 v[128:131], v[8:15], v[16:23], v[196:199], v144, v144 op_sel:[0,1,0] op_sel_hi:[0,0,0]
	s_waitcnt lgkmcnt(4)
	v_mfma_scale_f32_16x16x128_f8f6f4 v[124:127], v[0:7], v[24:31], v[200:203], v144, v144 op_sel:[0,1,0] op_sel_hi:[0,0,0]
	v_mfma_scale_f32_16x16x128_f8f6f4 v[116:119], v[8:15], v[24:31], v[116:119], v144, v144 op_sel:[0,1,0] op_sel_hi:[0,0,0]
	s_waitcnt lgkmcnt(1)
	v_mfma_scale_f32_16x16x128_f8f6f4 v[108:111], v[0:7], v[32:39], v[108:111], v144, v144 op_sel:[0,1,0] op_sel_hi:[0,0,0]
	v_mfma_scale_f32_16x16x128_f8f6f4 v[100:103], v[8:15], v[32:39], v[204:207], v144, v144 op_sel:[0,1,0] op_sel_hi:[0,0,0]
	s_waitcnt lgkmcnt(0)
	v_mfma_scale_f32_16x16x128_f8f6f4 v[92:95], v[0:7], v[40:47], v[208:211], v144, v144 op_sel:[0,1,0] op_sel_hi:[0,0,0]
	v_mfma_scale_f32_16x16x128_f8f6f4 v[84:87], v[8:15], v[40:47], v[212:215], v144, v144 op_sel:[0,1,0] op_sel_hi:[0,0,0]
	s_setprio 0
	s_barrier
; #define G_WAIT_V(n) asm volatile("s_waitcnt vmcnt(" #n ")" ::: "memory")
; #define G_WAIT_L(n) asm volatile("s_waitcnt lgkmcnt(" #n ")" ::: "memory")
; #define G_BAR do { asm volatile("" ::: "memory"); __builtin_amdgcn_s_barrier(); asm volatile("" ::: "memory"); } while (0)
; #define G_SCHED __builtin_amdgcn_sched_barrier(0)
; #define STG_A(b, h, kt) do { const unsigned char* _g = A + (size_t)KT_(kt) * ASTEP; \
;         dma16((const void*)(_g + (size_t)((h) * 128) * ROWB), ROWB ? aoff[0][0] : aoff[h][0], lds_u + SA_(b, h) + dma0); \
;         dma16((const void*)(_g + (size_t)((h) * 128 + 64) * ROWB), ROWB ? aoff[0][0] : aoff[h][1], lds_u + SA_(b, h) + dma1); } while (0)
; #define STG_B(b, h, kt) do { const unsigned char* _g = img + (size_t)KT_(kt) * 32768 + (h) * 16384; \
;         dma16((const void*)(_g + dma0), boffl, lds_u + SB_(b, h) + dma0); \
;         dma16((const void*)(_g + dma1), boffl, lds_u + SB_(b, h) + dma1); } while (0)
; #define LDA_(dst, b, h) do { _Pragma("unroll") for (int _m = 0; _m < 4; ++_m) { \
;         dst[_m].lo = *(LAS3 const i32x4d*)(ap0 + SA_(b, h) + _m * 2048); \
;         dst[_m].hi = *(LAS3 const i32x4d*)(ap1 + SA_(b, h) + _m * 2048); } } while (0)
; #define LDBF(dst, b, h) do { _Pragma("unroll") for (int _n = 0; _n < 2; ++_n) { \
;         dst[_n].lo = *(LAS3 const i32x4d*)(bp0 + (SB_(b, h) - 4 * GHTB) + _n * 8192); \
;         dst[_n].hi = *(LAS3 const i32x4d*)(bp1 + (SB_(b, h) - 4 * GHTB) + _n * 8192); } } while (0)
;     ...
;         LDBF(B0, 1, 0); G_SCHED; LDA_(At, 1, 0); STG_A(0, 1, t2);
;         G_WAIT_L(8); G_BAR; G_WAIT_L(0); MMAD(0, 0, At, B0); G_BAR; G_SCHED;
;         LDBF(B1, 1, 1); STG_B(1, 0, t3);
;         G_BAR; G_WAIT_L(0); MMAD(0, 1, At, B1); G_BAR;
;         LDA_(At, 1, 1); STG_A(1, 0, t3);
;         G_BAR; G_WAIT_L(0); MMAD(1, 0, At, B0); G_BAR; G_SCHED;
;         STG_B(1, 1, t3);
;         G_WAIT_V(6); G_BAR; MMAD(1, 1, At, B1); G_BAR;
;     }
;     G_WAIT_V(0); G_WAIT_L(0);
	ds_read_b128 v[148:151], v139 offset:49152
	ds_read_b128 v[156:159], v139 offset:57344
	ds_read_b128 v[152:155], v140 offset:49152
	ds_read_b128 v[160:163], v140 offset:57344
	s_mov_b32 s58, m0
	s_mov_b32 m0, s60
	s_nop 2
	global_load_lds_dwordx4 v141, s[56:57]
	s_mov_b32 m0, s58
	s_mov_b32 s56, m0
	s_mov_b32 m0, s68
	s_nop 2
	global_load_lds_dwordx4 v141, s[54:55]
	s_mov_b32 m0, s56
	s_waitcnt vmcnt(10)
	s_barrier
	s_waitcnt lgkmcnt(0)
	s_setprio 1
	s_waitcnt lgkmcnt(1)
	v_mfma_scale_f32_16x16x128_f8f6f4 v[120:123], v[148:155], v[16:23], v[120:123], v144, v144 op_sel:[0,1,0] op_sel_hi:[0,0,0]
	s_waitcnt lgkmcnt(0)
	v_mfma_scale_f32_16x16x128_f8f6f4 v[112:115], v[156:163], v[16:23], v[112:115], v144, v144 op_sel:[0,1,0] op_sel_hi:[0,0,0]
	v_mfma_scale_f32_16x16x128_f8f6f4 v[104:107], v[148:155], v[24:31], v[104:107], v144, v144 op_sel:[0,1,0] op_sel_hi:[0,0,0]
	v_mfma_scale_f32_16x16x128_f8f6f4 v[96:99], v[156:163], v[24:31], v[164:167], v144, v144 op_sel:[0,1,0] op_sel_hi:[0,0,0]
	v_mfma_scale_f32_16x16x128_f8f6f4 v[88:91], v[148:155], v[32:39], v[168:171], v144, v144 op_sel:[0,1,0] op_sel_hi:[0,0,0]
	v_mfma_scale_f32_16x16x128_f8f6f4 v[80:83], v[156:163], v[32:39], v[172:175], v144, v144 op_sel:[0,1,0] op_sel_hi:[0,0,0]
	v_mfma_scale_f32_16x16x128_f8f6f4 v[76:79], v[148:155], v[40:47], v[176:179], v144, v144 op_sel:[0,1,0] op_sel_hi:[0,0,0]
	v_mfma_scale_f32_16x16x128_f8f6f4 v[72:75], v[156:163], v[40:47], v[180:183], v144, v144 op_sel:[0,1,0] op_sel_hi:[0,0,0]
	s_setprio 0
	s_barrier
	ds_read_b128 v[16:19], v137 offset:49152
	ds_read_b128 v[164:167], v137 offset:51200
	ds_read_b128 v[20:23], v138 offset:49152
	ds_read_b128 v[168:171], v138 offset:51200
	ds_read_b128 v[172:175], v137 offset:53248
	ds_read_b128 v[180:183], v137 offset:55296
	ds_read_b128 v[176:179], v138 offset:53248
	ds_read_b128 v[184:187], v138 offset:55296
	s_mov_b32 s54, m0
	s_mov_b32 m0, s90
	s_nop 2
	global_load_lds_dwordx4 v136, s[48:49]
	s_mov_b32 m0, s54
	s_mov_b32 s48, m0
	s_mov_b32 m0, s88
	s_nop 2
	global_load_lds_dwordx4 v136, s[36:37]
	s_mov_b32 m0, s48
	s_barrier
	s_waitcnt lgkmcnt(0)
	s_setprio 1
	s_waitcnt lgkmcnt(5)
	v_mfma_scale_f32_16x16x128_f8f6f4 v[68:71], v[0:7], v[16:23], v[68:71], v144, v144 op_sel:[0,1,0] op_sel_hi:[0,0,0]
	v_mfma_scale_f32_16x16x128_f8f6f4 v[64:67], v[8:15], v[16:23], v[64:67], v144, v144 op_sel:[0,1,0] op_sel_hi:[0,0,0]
	s_waitcnt lgkmcnt(4)
	v_mfma_scale_f32_16x16x128_f8f6f4 v[60:63], v[0:7], v[164:171], v[60:63], v144, v144 op_sel:[0,1,0] op_sel_hi:[0,0,0]
	v_mfma_scale_f32_16x16x128_f8f6f4 v[52:55], v[8:15], v[164:171], v[52:55], v144, v144 op_sel:[0,1,0] op_sel_hi:[0,0,0]
	s_waitcnt lgkmcnt(1)
	v_mfma_scale_f32_16x16x128_f8f6f4 v[44:47], v[0:7], v[172:179], v[216:219], v144, v144 op_sel:[0,1,0] op_sel_hi:[0,0,0]
	v_mfma_scale_f32_16x16x128_f8f6f4 v[40:43], v[8:15], v[172:179], v[220:223], v144, v144 op_sel:[0,1,0] op_sel_hi:[0,0,0]
	s_waitcnt lgkmcnt(0)
	v_mfma_scale_f32_16x16x128_f8f6f4 v[28:31], v[0:7], v[180:187], v[224:227], v144, v144 op_sel:[0,1,0] op_sel_hi:[0,0,0]
	v_mfma_scale_f32_16x16x128_f8f6f4 v[24:27], v[8:15], v[180:187], v[228:231], v144, v144 op_sel:[0,1,0] op_sel_hi:[0,0,0]
	s_setprio 0
	s_barrier
	s_mov_b32 s36, m0
	s_mov_b32 m0, s33
	s_nop 2
	global_load_lds_dwordx4 v141, s[34:35]
	s_mov_b32 m0, s36
	s_mov_b32 s34, m0
	s_mov_b32 m0, s6
	s_nop 2
	global_load_lds_dwordx4 v141, s[30:31]
	s_mov_b32 m0, s34
	s_waitcnt vmcnt(10)
	s_barrier
	s_setprio 1
	v_mfma_scale_f32_16x16x128_f8f6f4 v[56:59], v[148:155], v[16:23], v[56:59], v144, v144 op_sel:[0,1,0] op_sel_hi:[0,0,0]
	v_mfma_scale_f32_16x16x128_f8f6f4 v[48:51], v[156:163], v[16:23], v[48:51], v144, v144 op_sel:[0,1,0] op_sel_hi:[0,0,0]
	v_mfma_scale_f32_16x16x128_f8f6f4 v[36:39], v[148:155], v[164:171], v[232:235], v144, v144 op_sel:[0,1,0] op_sel_hi:[0,0,0]
	v_mfma_scale_f32_16x16x128_f8f6f4 v[32:35], v[156:163], v[164:171], v[236:239], v144, v144 op_sel:[0,1,0] op_sel_hi:[0,0,0]
	v_mfma_scale_f32_16x16x128_f8f6f4 v[20:23], v[148:155], v[172:179], v[240:243], v144, v144 op_sel:[0,1,0] op_sel_hi:[0,0,0]
	v_mfma_scale_f32_16x16x128_f8f6f4 v[16:19], v[156:163], v[172:179], v[244:247], v144, v144 op_sel:[0,1,0] op_sel_hi:[0,0,0]
	v_mfma_scale_f32_16x16x128_f8f6f4 v[12:15], v[148:155], v[180:187], v[248:251], v144, v144 op_sel:[0,1,0] op_sel_hi:[0,0,0]
	v_mfma_scale_f32_16x16x128_f8f6f4 v[8:11], v[156:163], v[180:187], v[188:191], v144, v144 op_sel:[0,1,0] op_sel_hi:[0,0,0]
	s_setprio 0
	s_barrier
	s_mov_b32 vcc_hi, vcc_lo
	s_cbranch_scc0 .LBB0_562
	s_waitcnt vmcnt(0)
	s_waitcnt lgkmcnt(0)
	s_mov_b32 s0, s38
	s_mov_b32 s72, s83
	s_mov_b32 s70, s82
	s_mov_b32 s61, s79
	s_mov_b32 s59, s89
	s_mov_b32 s77, s38
	s_cmp_eq_u32 s0, 0
	s_cbranch_scc0 .LBB0_565
	s_barrier

; #define LAS3 __attribute__((address_space(3)))
; #define LAS __attribute__((address_space(3)))
; __global__ void __launch_bounds__(512, 2) k_mega(Params p) {
;     extern __shared__ __attribute__((aligned(16))) char smem[];
;     LAS3 char* lds = (LAS3 char*)smem;
;     volatile LAS unsigned* xbw = (volatile LAS unsigned*)(lds + LDS_MISC);
;     int wid = __builtin_amdgcn_readfirstlane((int)(threadIdx.x >> 6)); asm volatile("" : "+s"(wid));
	.amdhsa_kernel _ZN12_GLOBAL__N_16k_megaENS_6ParamsE
		.amdhsa_group_segment_fixed_size 0
		.amdhsa_private_segment_fixed_size 0
		.amdhsa_kernarg_size 576
		.amdhsa_user_sgpr_count 2
		.amdhsa_user_sgpr_dispatch_ptr 0
		.amdhsa_user_sgpr_queue_ptr 0
		.amdhsa_user_sgpr_kernarg_segment_ptr 1
		.amdhsa_user_sgpr_dispatch_id 0
		.amdhsa_user_sgpr_kernarg_preload_length 0
		.amdhsa_user_sgpr_kernarg_preload_offset 0
		.amdhsa_user_sgpr_private_segment_size 0
		.amdhsa_uses_dynamic_stack 0
		.amdhsa_enable_private_segment 0
		.amdhsa_system_sgpr_workgroup_id_x 1
		.amdhsa_system_sgpr_workgroup_id_y 0
		.amdhsa_system_sgpr_workgroup_id_z 0
		.amdhsa_system_sgpr_workgroup_info 0
		.amdhsa_system_vgpr_workitem_id 0
		.amdhsa_next_free_vgpr 256
		.amdhsa_next_free_sgpr 102
		.amdhsa_accum_offset 256
		.amdhsa_reserve_vcc 1
		.amdhsa_float_round_mode_32 0
		.amdhsa_float_round_mode_16_64 0
		.amdhsa_float_denorm_mode_32 3
		.amdhsa_float_denorm_mode_16_64 3
		.amdhsa_dx10_clamp 1
		.amdhsa_ieee_mode 1
		.amdhsa_fp16_overflow 0
		.amdhsa_tg_split 0
		.amdhsa_exception_fp_ieee_invalid_op 0
		.amdhsa_exception_fp_denorm_src 0
		.amdhsa_exception_fp_ieee_div_zero 0
		.amdhsa_exception_fp_ieee_overflow 0
		.amdhsa_exception_fp_ieee_underflow 0
		.amdhsa_exception_fp_ieee_inexact 0
		.amdhsa_exception_int_div_zero 0
	.end_amdhsa_kernel

; #define LAS3 __attribute__((address_space(3)))
; #define LAS __attribute__((address_space(3)))
; __global__ void __launch_bounds__(512, 2) k_mega(Params p) {
;     extern __shared__ __attribute__((aligned(16))) char smem[];
;     LAS3 char* lds = (LAS3 char*)smem;
;     volatile LAS unsigned* xbw = (volatile LAS unsigned*)(lds + LDS_MISC);
;     int wid = __builtin_amdgcn_readfirstlane((int)(threadIdx.x >> 6)); asm volatile("" : "+s"(wid));
amdhsa.kernels:
  - .agpr_count:     0
    .args:
      - .offset:         0
        .size:           320
        .value_kind:     by_value
      - .offset:         320
        .size:           4
        .value_kind:     hidden_block_count_x
      - .offset:         324
        .size:           4
        .value_kind:     hidden_block_count_y
      - .offset:         328
        .size:           4
        .value_kind:     hidden_block_count_z
      - .offset:         332
        .size:           2
        .value_kind:     hidden_group_size_x
      - .offset:         334
        .size:           2
        .value_kind:     hidden_group_size_y
      - .offset:         336
        .size:           2
        .value_kind:     hidden_group_size_z
      - .offset:         338
        .size:           2
        .value_kind:     hidden_remainder_x
      - .offset:         340
        .size:           2
        .value_kind:     hidden_remainder_y
      - .offset:         342
        .size:           2
        .value_kind:     hidden_remainder_z
      - .offset:         360
        .size:           8
        .value_kind:     hidden_global_offset_x
      - .offset:         368
        .size:           8
        .value_kind:     hidden_global_offset_y
      - .offset:         376
        .size:           8
        .value_kind:     hidden_global_offset_z
      - .offset:         384
        .size:           2
        .value_kind:     hidden_grid_dims
      - .offset:         440
        .size:           4
        .value_kind:     hidden_dynamic_lds_size
    .group_segment_fixed_size: 0
    .kernarg_segment_align: 8
    .kernarg_segment_size: 576
    .language:       OpenCL C
    .language_version:
      - 2
      - 0
    .max_flat_workgroup_size: 512
    .name:           _ZN12_GLOBAL__N_16k_megaENS_6ParamsE
    .private_segment_fixed_size: 0
    .sgpr_count:     108
    .sgpr_spill_count: 105
    .symbol:         _ZN12_GLOBAL__N_16k_megaENS_6ParamsE.kd
    .uniform_work_group_size: 1
    .uses_dynamic_stack: false
    .vgpr_count:     256
    .vgpr_spill_count: 0
    .wavefront_size: 64
